# phase 3 scans: each batch of recurrence steps issues its loads together (counted vmcnt) instead of a vmcnt(0) round trip per load; plus the lists-phase change
# speedup vs baseline: 1.0066x; 1.0025x over previous
.LBB0_458:
	s_waitcnt lgkmcnt(0)
	v_lshl_add_u64 v[18:19], s[8:9], 0, v[4:5]
	v_add_co_u32_e32 v18, vcc, 0x52200000, v18
	s_nop 1
	v_addc_co_u32_e32 v19, vcc, 0, v19, vcc
	v_lshl_add_u64 v[22:23], s[8:9], 0, v[2:3]
	v_add_co_u32_e32 v22, vcc, 0x70400000, v22
	s_nop 1
	v_addc_co_u32_e32 v23, vcc, 0, v23, vcc
	v_mov_b32_e32 v20, v18
	v_mov_b32_e32 v21, v19
	v_add_co_u32_e32 v20, vcc, 0x8000000, v20
	s_nop 1
	v_addc_co_u32_e32 v21, vcc, 0, v21, vcc
	global_load_dwordx2 v[32:33], v[18:19], off
	v_add_co_u32_e32 v18, vcc, 0x10000, v18
	s_nop 1
	v_addc_co_u32_e32 v19, vcc, 0, v19, vcc
	global_load_dwordx4 v[64:67], v[22:23], off
	global_load_dwordx2 v[34:35], v[18:19], off
	v_add_co_u32_e32 v18, vcc, 0x10000, v18
	s_nop 1
	v_addc_co_u32_e32 v19, vcc, 0, v19, vcc
	global_load_dwordx4 v[68:71], v[22:23], off offset:512
	global_load_dwordx2 v[36:37], v[18:19], off
	v_add_co_u32_e32 v18, vcc, 0x10000, v18
	s_nop 1
	v_addc_co_u32_e32 v19, vcc, 0, v19, vcc
	global_load_dwordx4 v[72:75], v[22:23], off offset:1024
	global_load_dwordx2 v[38:39], v[18:19], off
	v_add_co_u32_e32 v18, vcc, 0x10000, v18
	s_nop 1
	v_addc_co_u32_e32 v19, vcc, 0, v19, vcc
	global_load_dwordx4 v[76:79], v[22:23], off offset:1536
	global_load_dwordx2 v[40:41], v[18:19], off
	v_add_co_u32_e32 v18, vcc, 0x10000, v18
	s_nop 1
	v_addc_co_u32_e32 v19, vcc, 0, v19, vcc
	global_load_dwordx4 v[80:83], v[22:23], off offset:2048
	global_load_dwordx2 v[42:43], v[18:19], off
	v_add_co_u32_e32 v18, vcc, 0x10000, v18
	s_nop 1
	v_addc_co_u32_e32 v19, vcc, 0, v19, vcc
	global_load_dwordx4 v[84:87], v[22:23], off offset:2560
	global_load_dwordx2 v[44:45], v[18:19], off
	v_add_co_u32_e32 v18, vcc, 0x10000, v18
	s_nop 1
	v_addc_co_u32_e32 v19, vcc, 0, v19, vcc
	global_load_dwordx4 v[88:91], v[22:23], off offset:3072
	global_load_dwordx2 v[46:47], v[18:19], off
	v_add_co_u32_e32 v18, vcc, 0x10000, v18
	s_nop 1
	v_addc_co_u32_e32 v19, vcc, 0, v19, vcc
	global_load_dwordx4 v[92:95], v[22:23], off offset:3584
	v_add_co_u32_e32 v22, vcc, 0x1000, v22
	s_nop 1
	v_addc_co_u32_e32 v23, vcc, 0, v23, vcc
	global_load_dwordx2 v[48:49], v[18:19], off
	v_add_co_u32_e32 v18, vcc, 0x10000, v18
	s_nop 1
	v_addc_co_u32_e32 v19, vcc, 0, v19, vcc
	global_load_dwordx4 v[96:99], v[22:23], off
	global_load_dwordx2 v[50:51], v[18:19], off
	v_add_co_u32_e32 v18, vcc, 0x10000, v18
	s_nop 1
	v_addc_co_u32_e32 v19, vcc, 0, v19, vcc
	global_load_dwordx4 v[100:103], v[22:23], off offset:512
	global_load_dwordx2 v[52:53], v[18:19], off
	v_add_co_u32_e32 v18, vcc, 0x10000, v18
	s_nop 1
	v_addc_co_u32_e32 v19, vcc, 0, v19, vcc
	global_load_dwordx4 v[104:107], v[22:23], off offset:1024
	global_load_dwordx2 v[54:55], v[18:19], off
	v_add_co_u32_e32 v18, vcc, 0x10000, v18
	s_nop 1
	v_addc_co_u32_e32 v19, vcc, 0, v19, vcc
	global_load_dwordx4 v[108:111], v[22:23], off offset:1536
	global_load_dwordx2 v[56:57], v[18:19], off
	v_add_co_u32_e32 v18, vcc, 0x10000, v18
	s_nop 1
	v_addc_co_u32_e32 v19, vcc, 0, v19, vcc
	global_load_dwordx4 v[112:115], v[22:23], off offset:2048
	global_load_dwordx2 v[58:59], v[18:19], off
	v_add_co_u32_e32 v18, vcc, 0x10000, v18
	s_nop 1
	v_addc_co_u32_e32 v19, vcc, 0, v19, vcc
	global_load_dwordx4 v[116:119], v[22:23], off offset:2560
	global_load_dwordx2 v[60:61], v[18:19], off
	v_add_co_u32_e32 v18, vcc, 0x10000, v18
	s_nop 1
	v_addc_co_u32_e32 v19, vcc, 0, v19, vcc
	global_load_dwordx4 v[120:123], v[22:23], off offset:3072
	global_load_dwordx2 v[62:63], v[18:19], off
	v_add_co_u32_e32 v18, vcc, 0x10000, v18
	s_nop 1
	v_addc_co_u32_e32 v19, vcc, 0, v19, vcc
	global_load_dwordx4 v[124:127], v[22:23], off offset:3584
	v_add_co_u32_e32 v22, vcc, 0x1000, v22
	s_nop 1
	v_addc_co_u32_e32 v23, vcc, 0, v23, vcc
	s_waitcnt vmcnt(30)
	v_cvt_pk_bf16_f32 v28, v10, v11
	v_cvt_pk_bf16_f32 v29, v12, v13
	global_store_dwordx2 v[20:21], v[28:29], off
	v_add_co_u32_e32 v20, vcc, 0x10000, v20
	s_nop 1
	v_addc_co_u32_e32 v21, vcc, 0, v21, vcc
	v_lshlrev_b32_e32 v24, 16, v32
	v_and_b32_e32 v25, 0xffff0000, v32
	v_lshlrev_b32_e32 v26, 16, v33
	v_and_b32_e32 v27, 0xffff0000, v33
	v_pk_fma_f32 v[10:11], v[10:11], v[64:65], v[24:25]
	v_pk_fma_f32 v[12:13], v[12:13], v[66:67], v[26:27]
	s_waitcnt vmcnt(29)
	v_cvt_pk_bf16_f32 v28, v10, v11
	v_cvt_pk_bf16_f32 v29, v12, v13
	global_store_dwordx2 v[20:21], v[28:29], off
	v_add_co_u32_e32 v20, vcc, 0x10000, v20
	s_nop 1
	v_addc_co_u32_e32 v21, vcc, 0, v21, vcc
	v_lshlrev_b32_e32 v24, 16, v34
	v_and_b32_e32 v25, 0xffff0000, v34
	v_lshlrev_b32_e32 v26, 16, v35
	v_and_b32_e32 v27, 0xffff0000, v35
	v_pk_fma_f32 v[10:11], v[10:11], v[68:69], v[24:25]
	v_pk_fma_f32 v[12:13], v[12:13], v[70:71], v[26:27]
	s_waitcnt vmcnt(28)
	v_cvt_pk_bf16_f32 v28, v10, v11
	v_cvt_pk_bf16_f32 v29, v12, v13
	global_store_dwordx2 v[20:21], v[28:29], off
	v_add_co_u32_e32 v20, vcc, 0x10000, v20
	s_nop 1
	v_addc_co_u32_e32 v21, vcc, 0, v21, vcc
	v_lshlrev_b32_e32 v24, 16, v36
	v_and_b32_e32 v25, 0xffff0000, v36
	v_lshlrev_b32_e32 v26, 16, v37
	v_and_b32_e32 v27, 0xffff0000, v37
	v_pk_fma_f32 v[10:11], v[10:11], v[72:73], v[24:25]
	v_pk_fma_f32 v[12:13], v[12:13], v[74:75], v[26:27]
	s_waitcnt vmcnt(27)
	v_cvt_pk_bf16_f32 v28, v10, v11
	v_cvt_pk_bf16_f32 v29, v12, v13
	global_store_dwordx2 v[20:21], v[28:29], off
	v_add_co_u32_e32 v20, vcc, 0x10000, v20
	s_nop 1
	v_addc_co_u32_e32 v21, vcc, 0, v21, vcc
	v_lshlrev_b32_e32 v24, 16, v38
	v_and_b32_e32 v25, 0xffff0000, v38
	v_lshlrev_b32_e32 v26, 16, v39
	v_and_b32_e32 v27, 0xffff0000, v39
	v_pk_fma_f32 v[10:11], v[10:11], v[76:77], v[24:25]
	v_pk_fma_f32 v[12:13], v[12:13], v[78:79], v[26:27]
	s_waitcnt vmcnt(26)
	v_cvt_pk_bf16_f32 v28, v10, v11
	v_cvt_pk_bf16_f32 v29, v12, v13
	global_store_dwordx2 v[20:21], v[28:29], off
	v_add_co_u32_e32 v20, vcc, 0x10000, v20
	s_nop 1
	v_addc_co_u32_e32 v21, vcc, 0, v21, vcc
	v_lshlrev_b32_e32 v24, 16, v40
	v_and_b32_e32 v25, 0xffff0000, v40
	v_lshlrev_b32_e32 v26, 16, v41
	v_and_b32_e32 v27, 0xffff0000, v41
	v_pk_fma_f32 v[10:11], v[10:11], v[80:81], v[24:25]
	v_pk_fma_f32 v[12:13], v[12:13], v[82:83], v[26:27]
	s_waitcnt vmcnt(25)
	v_cvt_pk_bf16_f32 v28, v10, v11
	v_cvt_pk_bf16_f32 v29, v12, v13
	global_store_dwordx2 v[20:21], v[28:29], off
	v_add_co_u32_e32 v20, vcc, 0x10000, v20
	s_nop 1
	v_addc_co_u32_e32 v21, vcc, 0, v21, vcc
	v_lshlrev_b32_e32 v24, 16, v42
	v_and_b32_e32 v25, 0xffff0000, v42
	v_lshlrev_b32_e32 v26, 16, v43
	v_and_b32_e32 v27, 0xffff0000, v43
	v_pk_fma_f32 v[10:11], v[10:11], v[84:85], v[24:25]
	v_pk_fma_f32 v[12:13], v[12:13], v[86:87], v[26:27]
	s_waitcnt vmcnt(24)
	v_cvt_pk_bf16_f32 v28, v10, v11
	v_cvt_pk_bf16_f32 v29, v12, v13
	global_store_dwordx2 v[20:21], v[28:29], off
	v_add_co_u32_e32 v20, vcc, 0x10000, v20
	s_nop 1
	v_addc_co_u32_e32 v21, vcc, 0, v21, vcc
	v_lshlrev_b32_e32 v24, 16, v44
	v_and_b32_e32 v25, 0xffff0000, v44
	v_lshlrev_b32_e32 v26, 16, v45
	v_and_b32_e32 v27, 0xffff0000, v45
	v_pk_fma_f32 v[10:11], v[10:11], v[88:89], v[24:25]
	v_pk_fma_f32 v[12:13], v[12:13], v[90:91], v[26:27]
	s_waitcnt vmcnt(23)
	v_cvt_pk_bf16_f32 v28, v10, v11
	v_cvt_pk_bf16_f32 v29, v12, v13
	global_store_dwordx2 v[20:21], v[28:29], off
	v_add_co_u32_e32 v20, vcc, 0x10000, v20
	s_nop 1
	v_addc_co_u32_e32 v21, vcc, 0, v21, vcc
	v_lshlrev_b32_e32 v24, 16, v46
	v_and_b32_e32 v25, 0xffff0000, v46
	v_lshlrev_b32_e32 v26, 16, v47
	v_and_b32_e32 v27, 0xffff0000, v47
	v_pk_fma_f32 v[10:11], v[10:11], v[92:93], v[24:25]
	v_pk_fma_f32 v[12:13], v[12:13], v[94:95], v[26:27]
	s_waitcnt vmcnt(22)
	v_cvt_pk_bf16_f32 v28, v10, v11
	v_cvt_pk_bf16_f32 v29, v12, v13
	global_store_dwordx2 v[20:21], v[28:29], off
	v_add_co_u32_e32 v20, vcc, 0x10000, v20
	s_nop 1
	v_addc_co_u32_e32 v21, vcc, 0, v21, vcc
	v_lshlrev_b32_e32 v24, 16, v48
	v_and_b32_e32 v25, 0xffff0000, v48
	v_lshlrev_b32_e32 v26, 16, v49
	v_and_b32_e32 v27, 0xffff0000, v49
	v_pk_fma_f32 v[10:11], v[10:11], v[96:97], v[24:25]
	v_pk_fma_f32 v[12:13], v[12:13], v[98:99], v[26:27]
	s_waitcnt vmcnt(21)
	v_cvt_pk_bf16_f32 v28, v10, v11
	v_cvt_pk_bf16_f32 v29, v12, v13
	global_store_dwordx2 v[20:21], v[28:29], off
	v_add_co_u32_e32 v20, vcc, 0x10000, v20
	s_nop 1
	v_addc_co_u32_e32 v21, vcc, 0, v21, vcc
	v_lshlrev_b32_e32 v24, 16, v50
	v_and_b32_e32 v25, 0xffff0000, v50
	v_lshlrev_b32_e32 v26, 16, v51
	v_and_b32_e32 v27, 0xffff0000, v51
	v_pk_fma_f32 v[10:11], v[10:11], v[100:101], v[24:25]
	v_pk_fma_f32 v[12:13], v[12:13], v[102:103], v[26:27]
	s_waitcnt vmcnt(20)
	v_cvt_pk_bf16_f32 v28, v10, v11
	v_cvt_pk_bf16_f32 v29, v12, v13
	global_store_dwordx2 v[20:21], v[28:29], off
	v_add_co_u32_e32 v20, vcc, 0x10000, v20
	s_nop 1
	v_addc_co_u32_e32 v21, vcc, 0, v21, vcc
	v_lshlrev_b32_e32 v24, 16, v52
	v_and_b32_e32 v25, 0xffff0000, v52
	v_lshlrev_b32_e32 v26, 16, v53
	v_and_b32_e32 v27, 0xffff0000, v53
	v_pk_fma_f32 v[10:11], v[10:11], v[104:105], v[24:25]
	v_pk_fma_f32 v[12:13], v[12:13], v[106:107], v[26:27]
	s_waitcnt vmcnt(19)
	v_cvt_pk_bf16_f32 v28, v10, v11
	v_cvt_pk_bf16_f32 v29, v12, v13
	global_store_dwordx2 v[20:21], v[28:29], off
	v_add_co_u32_e32 v20, vcc, 0x10000, v20
	s_nop 1
	v_addc_co_u32_e32 v21, vcc, 0, v21, vcc
	v_lshlrev_b32_e32 v24, 16, v54
	v_and_b32_e32 v25, 0xffff0000, v54
	v_lshlrev_b32_e32 v26, 16, v55
	v_and_b32_e32 v27, 0xffff0000, v55
	v_pk_fma_f32 v[10:11], v[10:11], v[108:109], v[24:25]
	v_pk_fma_f32 v[12:13], v[12:13], v[110:111], v[26:27]
	s_waitcnt vmcnt(18)
	v_cvt_pk_bf16_f32 v28, v10, v11
	v_cvt_pk_bf16_f32 v29, v12, v13
	global_store_dwordx2 v[20:21], v[28:29], off
	v_add_co_u32_e32 v20, vcc, 0x10000, v20
	s_nop 1
	v_addc_co_u32_e32 v21, vcc, 0, v21, vcc
	v_lshlrev_b32_e32 v24, 16, v56
	v_and_b32_e32 v25, 0xffff0000, v56
	v_lshlrev_b32_e32 v26, 16, v57
	v_and_b32_e32 v27, 0xffff0000, v57
	v_pk_fma_f32 v[10:11], v[10:11], v[112:113], v[24:25]
	v_pk_fma_f32 v[12:13], v[12:13], v[114:115], v[26:27]
	s_waitcnt vmcnt(17)
	v_cvt_pk_bf16_f32 v28, v10, v11
	v_cvt_pk_bf16_f32 v29, v12, v13
	global_store_dwordx2 v[20:21], v[28:29], off
	v_add_co_u32_e32 v20, vcc, 0x10000, v20
	s_nop 1
	v_addc_co_u32_e32 v21, vcc, 0, v21, vcc
	v_lshlrev_b32_e32 v24, 16, v58
	v_and_b32_e32 v25, 0xffff0000, v58
	v_lshlrev_b32_e32 v26, 16, v59
	v_and_b32_e32 v27, 0xffff0000, v59
	v_pk_fma_f32 v[10:11], v[10:11], v[116:117], v[24:25]
	v_pk_fma_f32 v[12:13], v[12:13], v[118:119], v[26:27]
	s_waitcnt vmcnt(16)
	v_cvt_pk_bf16_f32 v28, v10, v11
	v_cvt_pk_bf16_f32 v29, v12, v13
	global_store_dwordx2 v[20:21], v[28:29], off
	v_add_co_u32_e32 v20, vcc, 0x10000, v20
	s_nop 1
	v_addc_co_u32_e32 v21, vcc, 0, v21, vcc
	v_lshlrev_b32_e32 v24, 16, v60
	v_and_b32_e32 v25, 0xffff0000, v60
	v_lshlrev_b32_e32 v26, 16, v61
	v_and_b32_e32 v27, 0xffff0000, v61
	v_pk_fma_f32 v[10:11], v[10:11], v[120:121], v[24:25]
	v_pk_fma_f32 v[12:13], v[12:13], v[122:123], v[26:27]
	s_waitcnt vmcnt(15)
	v_cvt_pk_bf16_f32 v28, v10, v11
	v_cvt_pk_bf16_f32 v29, v12, v13
	global_store_dwordx2 v[20:21], v[28:29], off
	v_add_co_u32_e32 v20, vcc, 0x10000, v20
	s_nop 1
	v_addc_co_u32_e32 v21, vcc, 0, v21, vcc
	v_lshlrev_b32_e32 v24, 16, v62
	v_and_b32_e32 v25, 0xffff0000, v62
	v_lshlrev_b32_e32 v26, 16, v63
	v_and_b32_e32 v27, 0xffff0000, v63
	v_pk_fma_f32 v[10:11], v[10:11], v[124:125], v[24:25]
	v_pk_fma_f32 v[12:13], v[12:13], v[126:127], v[26:27]
	global_load_dwordx2 v[32:33], v[18:19], off
	v_add_co_u32_e32 v18, vcc, 0x10000, v18
	s_nop 1
	v_addc_co_u32_e32 v19, vcc, 0, v19, vcc
	global_load_dwordx4 v[64:67], v[22:23], off
	global_load_dwordx2 v[34:35], v[18:19], off
	v_add_co_u32_e32 v18, vcc, 0x10000, v18
	s_nop 1
	v_addc_co_u32_e32 v19, vcc, 0, v19, vcc
	global_load_dwordx4 v[68:71], v[22:23], off offset:512
	global_load_dwordx2 v[36:37], v[18:19], off
	v_add_co_u32_e32 v18, vcc, 0x10000, v18
	s_nop 1
	v_addc_co_u32_e32 v19, vcc, 0, v19, vcc
	global_load_dwordx4 v[72:75], v[22:23], off offset:1024
	global_load_dwordx2 v[38:39], v[18:19], off
	v_add_co_u32_e32 v18, vcc, 0x10000, v18
	s_nop 1
	v_addc_co_u32_e32 v19, vcc, 0, v19, vcc
	global_load_dwordx4 v[76:79], v[22:23], off offset:1536
	global_load_dwordx2 v[40:41], v[18:19], off
	v_add_co_u32_e32 v18, vcc, 0x10000, v18
	s_nop 1
	v_addc_co_u32_e32 v19, vcc, 0, v19, vcc
	global_load_dwordx4 v[80:83], v[22:23], off offset:2048
	global_load_dwordx2 v[42:43], v[18:19], off
	v_add_co_u32_e32 v18, vcc, 0x10000, v18
	s_nop 1
	v_addc_co_u32_e32 v19, vcc, 0, v19, vcc
	global_load_dwordx4 v[84:87], v[22:23], off offset:2560
	global_load_dwordx2 v[44:45], v[18:19], off
	v_add_co_u32_e32 v18, vcc, 0x10000, v18
	s_nop 1
	v_addc_co_u32_e32 v19, vcc, 0, v19, vcc
	global_load_dwordx4 v[88:91], v[22:23], off offset:3072
	global_load_dwordx2 v[46:47], v[18:19], off
	v_add_co_u32_e32 v18, vcc, 0x10000, v18
	s_nop 1
	v_addc_co_u32_e32 v19, vcc, 0, v19, vcc
	global_load_dwordx4 v[92:95], v[22:23], off offset:3584
	v_add_co_u32_e32 v22, vcc, 0x1000, v22
	s_nop 1
	v_addc_co_u32_e32 v23, vcc, 0, v23, vcc
	global_load_dwordx2 v[48:49], v[18:19], off
	v_add_co_u32_e32 v18, vcc, 0x10000, v18
	s_nop 1
	v_addc_co_u32_e32 v19, vcc, 0, v19, vcc
	global_load_dwordx4 v[96:99], v[22:23], off
	global_load_dwordx2 v[50:51], v[18:19], off
	v_add_co_u32_e32 v18, vcc, 0x10000, v18
	s_nop 1
	v_addc_co_u32_e32 v19, vcc, 0, v19, vcc
	global_load_dwordx4 v[100:103], v[22:23], off offset:512
	global_load_dwordx2 v[52:53], v[18:19], off
	v_add_co_u32_e32 v18, vcc, 0x10000, v18
	s_nop 1
	v_addc_co_u32_e32 v19, vcc, 0, v19, vcc
	global_load_dwordx4 v[104:107], v[22:23], off offset:1024
	global_load_dwordx2 v[54:55], v[18:19], off
	v_add_co_u32_e32 v18, vcc, 0x10000, v18
	s_nop 1
	v_addc_co_u32_e32 v19, vcc, 0, v19, vcc
	global_load_dwordx4 v[108:111], v[22:23], off offset:1536
	global_load_dwordx2 v[56:57], v[18:19], off
	v_add_co_u32_e32 v18, vcc, 0x10000, v18
	s_nop 1
	v_addc_co_u32_e32 v19, vcc, 0, v19, vcc
	global_load_dwordx4 v[112:115], v[22:23], off offset:2048
	global_load_dwordx2 v[58:59], v[18:19], off
	v_add_co_u32_e32 v18, vcc, 0x10000, v18
	s_nop 1
	v_addc_co_u32_e32 v19, vcc, 0, v19, vcc
	global_load_dwordx4 v[116:119], v[22:23], off offset:2560
	global_load_dwordx2 v[60:61], v[18:19], off
	v_add_co_u32_e32 v18, vcc, 0x10000, v18
	s_nop 1
	v_addc_co_u32_e32 v19, vcc, 0, v19, vcc
	global_load_dwordx4 v[120:123], v[22:23], off offset:3072
	global_load_dwordx2 v[62:63], v[18:19], off
	v_add_co_u32_e32 v18, vcc, 0x10000, v18
	s_nop 1
	v_addc_co_u32_e32 v19, vcc, 0, v19, vcc
	global_load_dwordx4 v[124:127], v[22:23], off offset:3584
	v_add_co_u32_e32 v22, vcc, 0x1000, v22
	s_nop 1
	v_addc_co_u32_e32 v23, vcc, 0, v23, vcc
	s_waitcnt vmcnt(30)
	v_cvt_pk_bf16_f32 v28, v10, v11
	v_cvt_pk_bf16_f32 v29, v12, v13
	global_store_dwordx2 v[20:21], v[28:29], off
	v_add_co_u32_e32 v20, vcc, 0x10000, v20
	s_nop 1
	v_addc_co_u32_e32 v21, vcc, 0, v21, vcc
	v_lshlrev_b32_e32 v24, 16, v32
	v_and_b32_e32 v25, 0xffff0000, v32
	v_lshlrev_b32_e32 v26, 16, v33
	v_and_b32_e32 v27, 0xffff0000, v33
	v_pk_fma_f32 v[10:11], v[10:11], v[64:65], v[24:25]
	v_pk_fma_f32 v[12:13], v[12:13], v[66:67], v[26:27]
	s_waitcnt vmcnt(29)
	v_cvt_pk_bf16_f32 v28, v10, v11
	v_cvt_pk_bf16_f32 v29, v12, v13
	global_store_dwordx2 v[20:21], v[28:29], off
	v_add_co_u32_e32 v20, vcc, 0x10000, v20
	s_nop 1
	v_addc_co_u32_e32 v21, vcc, 0, v21, vcc
	v_lshlrev_b32_e32 v24, 16, v34
	v_and_b32_e32 v25, 0xffff0000, v34
	v_lshlrev_b32_e32 v26, 16, v35
	v_and_b32_e32 v27, 0xffff0000, v35
	v_pk_fma_f32 v[10:11], v[10:11], v[68:69], v[24:25]
	v_pk_fma_f32 v[12:13], v[12:13], v[70:71], v[26:27]
	s_waitcnt vmcnt(28)
	v_cvt_pk_bf16_f32 v28, v10, v11
	v_cvt_pk_bf16_f32 v29, v12, v13
	global_store_dwordx2 v[20:21], v[28:29], off
	v_add_co_u32_e32 v20, vcc, 0x10000, v20
	s_nop 1
	v_addc_co_u32_e32 v21, vcc, 0, v21, vcc
	v_lshlrev_b32_e32 v24, 16, v36
	v_and_b32_e32 v25, 0xffff0000, v36
	v_lshlrev_b32_e32 v26, 16, v37
	v_and_b32_e32 v27, 0xffff0000, v37
	v_pk_fma_f32 v[10:11], v[10:11], v[72:73], v[24:25]
	v_pk_fma_f32 v[12:13], v[12:13], v[74:75], v[26:27]
	s_waitcnt vmcnt(27)
	v_cvt_pk_bf16_f32 v28, v10, v11
	v_cvt_pk_bf16_f32 v29, v12, v13
	global_store_dwordx2 v[20:21], v[28:29], off
	v_add_co_u32_e32 v20, vcc, 0x10000, v20
	s_nop 1
	v_addc_co_u32_e32 v21, vcc, 0, v21, vcc
	v_lshlrev_b32_e32 v24, 16, v38
	v_and_b32_e32 v25, 0xffff0000, v38
	v_lshlrev_b32_e32 v26, 16, v39
	v_and_b32_e32 v27, 0xffff0000, v39
	v_pk_fma_f32 v[10:11], v[10:11], v[76:77], v[24:25]
	v_pk_fma_f32 v[12:13], v[12:13], v[78:79], v[26:27]
	s_waitcnt vmcnt(26)
	v_cvt_pk_bf16_f32 v28, v10, v11
	v_cvt_pk_bf16_f32 v29, v12, v13
	global_store_dwordx2 v[20:21], v[28:29], off
	v_add_co_u32_e32 v20, vcc, 0x10000, v20
	s_nop 1
	v_addc_co_u32_e32 v21, vcc, 0, v21, vcc
	v_lshlrev_b32_e32 v24, 16, v40
	v_and_b32_e32 v25, 0xffff0000, v40
	v_lshlrev_b32_e32 v26, 16, v41
	v_and_b32_e32 v27, 0xffff0000, v41
	v_pk_fma_f32 v[10:11], v[10:11], v[80:81], v[24:25]
	v_pk_fma_f32 v[12:13], v[12:13], v[82:83], v[26:27]
	s_waitcnt vmcnt(25)
	v_cvt_pk_bf16_f32 v28, v10, v11
	v_cvt_pk_bf16_f32 v29, v12, v13
	global_store_dwordx2 v[20:21], v[28:29], off
	v_add_co_u32_e32 v20, vcc, 0x10000, v20
	s_nop 1
	v_addc_co_u32_e32 v21, vcc, 0, v21, vcc
	v_lshlrev_b32_e32 v24, 16, v42
	v_and_b32_e32 v25, 0xffff0000, v42
	v_lshlrev_b32_e32 v26, 16, v43
	v_and_b32_e32 v27, 0xffff0000, v43
	v_pk_fma_f32 v[10:11], v[10:11], v[84:85], v[24:25]
	v_pk_fma_f32 v[12:13], v[12:13], v[86:87], v[26:27]
	s_waitcnt vmcnt(24)
	v_cvt_pk_bf16_f32 v28, v10, v11
	v_cvt_pk_bf16_f32 v29, v12, v13
	global_store_dwordx2 v[20:21], v[28:29], off
	v_add_co_u32_e32 v20, vcc, 0x10000, v20
	s_nop 1
	v_addc_co_u32_e32 v21, vcc, 0, v21, vcc
	v_lshlrev_b32_e32 v24, 16, v44
	v_and_b32_e32 v25, 0xffff0000, v44
	v_lshlrev_b32_e32 v26, 16, v45
	v_and_b32_e32 v27, 0xffff0000, v45
	v_pk_fma_f32 v[10:11], v[10:11], v[88:89], v[24:25]
	v_pk_fma_f32 v[12:13], v[12:13], v[90:91], v[26:27]
	s_waitcnt vmcnt(23)
	v_cvt_pk_bf16_f32 v28, v10, v11
	v_cvt_pk_bf16_f32 v29, v12, v13
	global_store_dwordx2 v[20:21], v[28:29], off
	v_add_co_u32_e32 v20, vcc, 0x10000, v20
	s_nop 1
	v_addc_co_u32_e32 v21, vcc, 0, v21, vcc
	v_lshlrev_b32_e32 v24, 16, v46
	v_and_b32_e32 v25, 0xffff0000, v46
	v_lshlrev_b32_e32 v26, 16, v47
	v_and_b32_e32 v27, 0xffff0000, v47
	v_pk_fma_f32 v[10:11], v[10:11], v[92:93], v[24:25]
	v_pk_fma_f32 v[12:13], v[12:13], v[94:95], v[26:27]
	s_waitcnt vmcnt(22)
	v_cvt_pk_bf16_f32 v28, v10, v11
	v_cvt_pk_bf16_f32 v29, v12, v13
	global_store_dwordx2 v[20:21], v[28:29], off
	v_add_co_u32_e32 v20, vcc, 0x10000, v20
	s_nop 1
	v_addc_co_u32_e32 v21, vcc, 0, v21, vcc
	v_lshlrev_b32_e32 v24, 16, v48
	v_and_b32_e32 v25, 0xffff0000, v48
	v_lshlrev_b32_e32 v26, 16, v49
	v_and_b32_e32 v27, 0xffff0000, v49
	v_pk_fma_f32 v[10:11], v[10:11], v[96:97], v[24:25]
	v_pk_fma_f32 v[12:13], v[12:13], v[98:99], v[26:27]
	s_waitcnt vmcnt(21)
	v_cvt_pk_bf16_f32 v28, v10, v11
	v_cvt_pk_bf16_f32 v29, v12, v13
	global_store_dwordx2 v[20:21], v[28:29], off
	v_add_co_u32_e32 v20, vcc, 0x10000, v20
	s_nop 1
	v_addc_co_u32_e32 v21, vcc, 0, v21, vcc
	v_lshlrev_b32_e32 v24, 16, v50
	v_and_b32_e32 v25, 0xffff0000, v50
	v_lshlrev_b32_e32 v26, 16, v51
	v_and_b32_e32 v27, 0xffff0000, v51
	v_pk_fma_f32 v[10:11], v[10:11], v[100:101], v[24:25]
	v_pk_fma_f32 v[12:13], v[12:13], v[102:103], v[26:27]
	s_waitcnt vmcnt(20)
	v_cvt_pk_bf16_f32 v28, v10, v11
	v_cvt_pk_bf16_f32 v29, v12, v13
	global_store_dwordx2 v[20:21], v[28:29], off
	v_add_co_u32_e32 v20, vcc, 0x10000, v20
	s_nop 1
	v_addc_co_u32_e32 v21, vcc, 0, v21, vcc
	v_lshlrev_b32_e32 v24, 16, v52
	v_and_b32_e32 v25, 0xffff0000, v52
	v_lshlrev_b32_e32 v26, 16, v53
	v_and_b32_e32 v27, 0xffff0000, v53
	v_pk_fma_f32 v[10:11], v[10:11], v[104:105], v[24:25]
	v_pk_fma_f32 v[12:13], v[12:13], v[106:107], v[26:27]
	s_waitcnt vmcnt(19)
	v_cvt_pk_bf16_f32 v28, v10, v11
	v_cvt_pk_bf16_f32 v29, v12, v13
	global_store_dwordx2 v[20:21], v[28:29], off
	v_add_co_u32_e32 v20, vcc, 0x10000, v20
	s_nop 1
	v_addc_co_u32_e32 v21, vcc, 0, v21, vcc
	v_lshlrev_b32_e32 v24, 16, v54
	v_and_b32_e32 v25, 0xffff0000, v54
	v_lshlrev_b32_e32 v26, 16, v55
	v_and_b32_e32 v27, 0xffff0000, v55
	v_pk_fma_f32 v[10:11], v[10:11], v[108:109], v[24:25]
	v_pk_fma_f32 v[12:13], v[12:13], v[110:111], v[26:27]
	s_waitcnt vmcnt(18)
	v_cvt_pk_bf16_f32 v28, v10, v11
	v_cvt_pk_bf16_f32 v29, v12, v13
	global_store_dwordx2 v[20:21], v[28:29], off
	v_add_co_u32_e32 v20, vcc, 0x10000, v20
	s_nop 1
	v_addc_co_u32_e32 v21, vcc, 0, v21, vcc
	v_lshlrev_b32_e32 v24, 16, v56
	v_and_b32_e32 v25, 0xffff0000, v56
	v_lshlrev_b32_e32 v26, 16, v57
	v_and_b32_e32 v27, 0xffff0000, v57
	v_pk_fma_f32 v[10:11], v[10:11], v[112:113], v[24:25]
	v_pk_fma_f32 v[12:13], v[12:13], v[114:115], v[26:27]
	s_waitcnt vmcnt(17)
	v_cvt_pk_bf16_f32 v28, v10, v11
	v_cvt_pk_bf16_f32 v29, v12, v13
	global_store_dwordx2 v[20:21], v[28:29], off
	v_add_co_u32_e32 v20, vcc, 0x10000, v20
	s_nop 1
	v_addc_co_u32_e32 v21, vcc, 0, v21, vcc
	v_lshlrev_b32_e32 v24, 16, v58
	v_and_b32_e32 v25, 0xffff0000, v58
	v_lshlrev_b32_e32 v26, 16, v59
	v_and_b32_e32 v27, 0xffff0000, v59
	v_pk_fma_f32 v[10:11], v[10:11], v[116:117], v[24:25]
	v_pk_fma_f32 v[12:13], v[12:13], v[118:119], v[26:27]
	s_waitcnt vmcnt(16)
	v_cvt_pk_bf16_f32 v28, v10, v11
	v_cvt_pk_bf16_f32 v29, v12, v13
	global_store_dwordx2 v[20:21], v[28:29], off
	v_add_co_u32_e32 v20, vcc, 0x10000, v20
	s_nop 1
	v_addc_co_u32_e32 v21, vcc, 0, v21, vcc
	v_lshlrev_b32_e32 v24, 16, v60
	v_and_b32_e32 v25, 0xffff0000, v60
	v_lshlrev_b32_e32 v26, 16, v61
	v_and_b32_e32 v27, 0xffff0000, v61
	v_pk_fma_f32 v[10:11], v[10:11], v[120:121], v[24:25]
	v_pk_fma_f32 v[12:13], v[12:13], v[122:123], v[26:27]
	s_waitcnt vmcnt(15)
	v_cvt_pk_bf16_f32 v28, v10, v11
	v_cvt_pk_bf16_f32 v29, v12, v13
	global_store_dwordx2 v[20:21], v[28:29], off
	v_add_co_u32_e32 v20, vcc, 0x10000, v20
	s_nop 1
	v_addc_co_u32_e32 v21, vcc, 0, v21, vcc
	v_lshlrev_b32_e32 v24, 16, v62
	v_and_b32_e32 v25, 0xffff0000, v62
	v_lshlrev_b32_e32 v26, 16, v63
	v_and_b32_e32 v27, 0xffff0000, v63
	v_pk_fma_f32 v[10:11], v[10:11], v[124:125], v[24:25]
	v_pk_fma_f32 v[12:13], v[12:13], v[126:127], v[26:27]
	global_load_dwordx2 v[32:33], v[18:19], off
	v_add_co_u32_e32 v18, vcc, 0x10000, v18
	s_nop 1
	v_addc_co_u32_e32 v19, vcc, 0, v19, vcc
	global_load_dwordx4 v[64:67], v[22:23], off
	global_load_dwordx2 v[34:35], v[18:19], off
	v_add_co_u32_e32 v18, vcc, 0x10000, v18
	s_nop 1
	v_addc_co_u32_e32 v19, vcc, 0, v19, vcc
	global_load_dwordx4 v[68:71], v[22:23], off offset:512
	global_load_dwordx2 v[36:37], v[18:19], off
	v_add_co_u32_e32 v18, vcc, 0x10000, v18
	s_nop 1
	v_addc_co_u32_e32 v19, vcc, 0, v19, vcc
	global_load_dwordx4 v[72:75], v[22:23], off offset:1024
	global_load_dwordx2 v[38:39], v[18:19], off
	v_add_co_u32_e32 v18, vcc, 0x10000, v18
	s_nop 1
	v_addc_co_u32_e32 v19, vcc, 0, v19, vcc
	global_load_dwordx4 v[76:79], v[22:23], off offset:1536
	global_load_dwordx2 v[40:41], v[18:19], off
	v_add_co_u32_e32 v18, vcc, 0x10000, v18
	s_nop 1
	v_addc_co_u32_e32 v19, vcc, 0, v19, vcc
	global_load_dwordx4 v[80:83], v[22:23], off offset:2048
	global_load_dwordx2 v[42:43], v[18:19], off
	v_add_co_u32_e32 v18, vcc, 0x10000, v18
	s_nop 1
	v_addc_co_u32_e32 v19, vcc, 0, v19, vcc
	global_load_dwordx4 v[84:87], v[22:23], off offset:2560
	global_load_dwordx2 v[44:45], v[18:19], off
	v_add_co_u32_e32 v18, vcc, 0x10000, v18
	s_nop 1
	v_addc_co_u32_e32 v19, vcc, 0, v19, vcc
	global_load_dwordx4 v[88:91], v[22:23], off offset:3072
	global_load_dwordx2 v[46:47], v[18:19], off
	v_add_co_u32_e32 v18, vcc, 0x10000, v18
	s_nop 1
	v_addc_co_u32_e32 v19, vcc, 0, v19, vcc
	global_load_dwordx4 v[92:95], v[22:23], off offset:3584
	v_add_co_u32_e32 v22, vcc, 0x1000, v22
	s_nop 1
	v_addc_co_u32_e32 v23, vcc, 0, v23, vcc
	global_load_dwordx2 v[48:49], v[18:19], off
	v_add_co_u32_e32 v18, vcc, 0x10000, v18
	s_nop 1
	v_addc_co_u32_e32 v19, vcc, 0, v19, vcc
	global_load_dwordx4 v[96:99], v[22:23], off
	global_load_dwordx2 v[50:51], v[18:19], off
	v_add_co_u32_e32 v18, vcc, 0x10000, v18
	s_nop 1
	v_addc_co_u32_e32 v19, vcc, 0, v19, vcc
	global_load_dwordx4 v[100:103], v[22:23], off offset:512
	global_load_dwordx2 v[52:53], v[18:19], off
	v_add_co_u32_e32 v18, vcc, 0x10000, v18
	s_nop 1
	v_addc_co_u32_e32 v19, vcc, 0, v19, vcc
	global_load_dwordx4 v[104:107], v[22:23], off offset:1024
	global_load_dwordx2 v[54:55], v[18:19], off
	v_add_co_u32_e32 v18, vcc, 0x10000, v18
	s_nop 1
	v_addc_co_u32_e32 v19, vcc, 0, v19, vcc
	global_load_dwordx4 v[108:111], v[22:23], off offset:1536
	global_load_dwordx2 v[56:57], v[18:19], off
	v_add_co_u32_e32 v18, vcc, 0x10000, v18
	s_nop 1
	v_addc_co_u32_e32 v19, vcc, 0, v19, vcc
	global_load_dwordx4 v[112:115], v[22:23], off offset:2048
	global_load_dwordx2 v[58:59], v[18:19], off
	v_add_co_u32_e32 v18, vcc, 0x10000, v18
	s_nop 1
	v_addc_co_u32_e32 v19, vcc, 0, v19, vcc
	global_load_dwordx4 v[116:119], v[22:23], off offset:2560
	global_load_dwordx2 v[60:61], v[18:19], off
	v_add_co_u32_e32 v18, vcc, 0x10000, v18
	s_nop 1
	v_addc_co_u32_e32 v19, vcc, 0, v19, vcc
	global_load_dwordx4 v[120:123], v[22:23], off offset:3072
	global_load_dwordx2 v[62:63], v[18:19], off
	v_add_co_u32_e32 v18, vcc, 0x10000, v18
	s_nop 1
	v_addc_co_u32_e32 v19, vcc, 0, v19, vcc
	global_load_dwordx4 v[124:127], v[22:23], off offset:3584
	v_add_co_u32_e32 v22, vcc, 0x1000, v22
	s_nop 1
	v_addc_co_u32_e32 v23, vcc, 0, v23, vcc
	s_waitcnt vmcnt(30)
	v_cvt_pk_bf16_f32 v28, v10, v11
	v_cvt_pk_bf16_f32 v29, v12, v13
	global_store_dwordx2 v[20:21], v[28:29], off
	v_add_co_u32_e32 v20, vcc, 0x10000, v20
	s_nop 1
	v_addc_co_u32_e32 v21, vcc, 0, v21, vcc
	v_lshlrev_b32_e32 v24, 16, v32
	v_and_b32_e32 v25, 0xffff0000, v32
	v_lshlrev_b32_e32 v26, 16, v33
	v_and_b32_e32 v27, 0xffff0000, v33
	v_pk_fma_f32 v[10:11], v[10:11], v[64:65], v[24:25]
	v_pk_fma_f32 v[12:13], v[12:13], v[66:67], v[26:27]
	s_waitcnt vmcnt(29)
	v_cvt_pk_bf16_f32 v28, v10, v11
	v_cvt_pk_bf16_f32 v29, v12, v13
	global_store_dwordx2 v[20:21], v[28:29], off
	v_add_co_u32_e32 v20, vcc, 0x10000, v20
	s_nop 1
	v_addc_co_u32_e32 v21, vcc, 0, v21, vcc
	v_lshlrev_b32_e32 v24, 16, v34
	v_and_b32_e32 v25, 0xffff0000, v34
	v_lshlrev_b32_e32 v26, 16, v35
	v_and_b32_e32 v27, 0xffff0000, v35
	v_pk_fma_f32 v[10:11], v[10:11], v[68:69], v[24:25]
	v_pk_fma_f32 v[12:13], v[12:13], v[70:71], v[26:27]
	s_waitcnt vmcnt(28)
	v_cvt_pk_bf16_f32 v28, v10, v11
	v_cvt_pk_bf16_f32 v29, v12, v13
	global_store_dwordx2 v[20:21], v[28:29], off
	v_add_co_u32_e32 v20, vcc, 0x10000, v20
	s_nop 1
	v_addc_co_u32_e32 v21, vcc, 0, v21, vcc
	v_lshlrev_b32_e32 v24, 16, v36
	v_and_b32_e32 v25, 0xffff0000, v36
	v_lshlrev_b32_e32 v26, 16, v37
	v_and_b32_e32 v27, 0xffff0000, v37
	v_pk_fma_f32 v[10:11], v[10:11], v[72:73], v[24:25]
	v_pk_fma_f32 v[12:13], v[12:13], v[74:75], v[26:27]
	s_waitcnt vmcnt(27)
	v_cvt_pk_bf16_f32 v28, v10, v11
	v_cvt_pk_bf16_f32 v29, v12, v13
	global_store_dwordx2 v[20:21], v[28:29], off
	v_add_co_u32_e32 v20, vcc, 0x10000, v20
	s_nop 1
	v_addc_co_u32_e32 v21, vcc, 0, v21, vcc
	v_lshlrev_b32_e32 v24, 16, v38
	v_and_b32_e32 v25, 0xffff0000, v38
	v_lshlrev_b32_e32 v26, 16, v39
	v_and_b32_e32 v27, 0xffff0000, v39
	v_pk_fma_f32 v[10:11], v[10:11], v[76:77], v[24:25]
	v_pk_fma_f32 v[12:13], v[12:13], v[78:79], v[26:27]
	s_waitcnt vmcnt(26)
	v_cvt_pk_bf16_f32 v28, v10, v11
	v_cvt_pk_bf16_f32 v29, v12, v13
	global_store_dwordx2 v[20:21], v[28:29], off
	v_add_co_u32_e32 v20, vcc, 0x10000, v20
	s_nop 1
	v_addc_co_u32_e32 v21, vcc, 0, v21, vcc
	v_lshlrev_b32_e32 v24, 16, v40
	v_and_b32_e32 v25, 0xffff0000, v40
	v_lshlrev_b32_e32 v26, 16, v41
	v_and_b32_e32 v27, 0xffff0000, v41
	v_pk_fma_f32 v[10:11], v[10:11], v[80:81], v[24:25]
	v_pk_fma_f32 v[12:13], v[12:13], v[82:83], v[26:27]
	s_waitcnt vmcnt(25)
	v_cvt_pk_bf16_f32 v28, v10, v11
	v_cvt_pk_bf16_f32 v29, v12, v13
	global_store_dwordx2 v[20:21], v[28:29], off
	v_add_co_u32_e32 v20, vcc, 0x10000, v20
	s_nop 1
	v_addc_co_u32_e32 v21, vcc, 0, v21, vcc
	v_lshlrev_b32_e32 v24, 16, v42
	v_and_b32_e32 v25, 0xffff0000, v42
	v_lshlrev_b32_e32 v26, 16, v43
	v_and_b32_e32 v27, 0xffff0000, v43
	v_pk_fma_f32 v[10:11], v[10:11], v[84:85], v[24:25]
	v_pk_fma_f32 v[12:13], v[12:13], v[86:87], v[26:27]
	s_waitcnt vmcnt(24)
	v_cvt_pk_bf16_f32 v28, v10, v11
	v_cvt_pk_bf16_f32 v29, v12, v13
	global_store_dwordx2 v[20:21], v[28:29], off
	v_add_co_u32_e32 v20, vcc, 0x10000, v20
	s_nop 1
	v_addc_co_u32_e32 v21, vcc, 0, v21, vcc
	v_lshlrev_b32_e32 v24, 16, v44
	v_and_b32_e32 v25, 0xffff0000, v44
	v_lshlrev_b32_e32 v26, 16, v45
	v_and_b32_e32 v27, 0xffff0000, v45
	v_pk_fma_f32 v[10:11], v[10:11], v[88:89], v[24:25]
	v_pk_fma_f32 v[12:13], v[12:13], v[90:91], v[26:27]
	s_waitcnt vmcnt(23)
	v_cvt_pk_bf16_f32 v28, v10, v11
	v_cvt_pk_bf16_f32 v29, v12, v13
	global_store_dwordx2 v[20:21], v[28:29], off
	v_add_co_u32_e32 v20, vcc, 0x10000, v20
	s_nop 1
	v_addc_co_u32_e32 v21, vcc, 0, v21, vcc
	v_lshlrev_b32_e32 v24, 16, v46
	v_and_b32_e32 v25, 0xffff0000, v46
	v_lshlrev_b32_e32 v26, 16, v47
	v_and_b32_e32 v27, 0xffff0000, v47
	v_pk_fma_f32 v[10:11], v[10:11], v[92:93], v[24:25]
	v_pk_fma_f32 v[12:13], v[12:13], v[94:95], v[26:27]
	s_waitcnt vmcnt(22)
	v_cvt_pk_bf16_f32 v28, v10, v11
	v_cvt_pk_bf16_f32 v29, v12, v13
	global_store_dwordx2 v[20:21], v[28:29], off
	v_add_co_u32_e32 v20, vcc, 0x10000, v20
	s_nop 1
	v_addc_co_u32_e32 v21, vcc, 0, v21, vcc
	v_lshlrev_b32_e32 v24, 16, v48
	v_and_b32_e32 v25, 0xffff0000, v48
	v_lshlrev_b32_e32 v26, 16, v49
	v_and_b32_e32 v27, 0xffff0000, v49
	v_pk_fma_f32 v[10:11], v[10:11], v[96:97], v[24:25]
	v_pk_fma_f32 v[12:13], v[12:13], v[98:99], v[26:27]
	s_waitcnt vmcnt(21)
	v_cvt_pk_bf16_f32 v28, v10, v11
	v_cvt_pk_bf16_f32 v29, v12, v13
	global_store_dwordx2 v[20:21], v[28:29], off
	v_add_co_u32_e32 v20, vcc, 0x10000, v20
	s_nop 1
	v_addc_co_u32_e32 v21, vcc, 0, v21, vcc
	v_lshlrev_b32_e32 v24, 16, v50
	v_and_b32_e32 v25, 0xffff0000, v50
	v_lshlrev_b32_e32 v26, 16, v51
	v_and_b32_e32 v27, 0xffff0000, v51
	v_pk_fma_f32 v[10:11], v[10:11], v[100:101], v[24:25]
	v_pk_fma_f32 v[12:13], v[12:13], v[102:103], v[26:27]
	s_waitcnt vmcnt(20)
	v_cvt_pk_bf16_f32 v28, v10, v11
	v_cvt_pk_bf16_f32 v29, v12, v13
	global_store_dwordx2 v[20:21], v[28:29], off
	v_add_co_u32_e32 v20, vcc, 0x10000, v20
	s_nop 1
	v_addc_co_u32_e32 v21, vcc, 0, v21, vcc
	v_lshlrev_b32_e32 v24, 16, v52
	v_and_b32_e32 v25, 0xffff0000, v52
	v_lshlrev_b32_e32 v26, 16, v53
	v_and_b32_e32 v27, 0xffff0000, v53
	v_pk_fma_f32 v[10:11], v[10:11], v[104:105], v[24:25]
	v_pk_fma_f32 v[12:13], v[12:13], v[106:107], v[26:27]
	s_waitcnt vmcnt(19)
	v_cvt_pk_bf16_f32 v28, v10, v11
	v_cvt_pk_bf16_f32 v29, v12, v13
	global_store_dwordx2 v[20:21], v[28:29], off
	v_add_co_u32_e32 v20, vcc, 0x10000, v20
	s_nop 1
	v_addc_co_u32_e32 v21, vcc, 0, v21, vcc
	v_lshlrev_b32_e32 v24, 16, v54
	v_and_b32_e32 v25, 0xffff0000, v54
	v_lshlrev_b32_e32 v26, 16, v55
	v_and_b32_e32 v27, 0xffff0000, v55
	v_pk_fma_f32 v[10:11], v[10:11], v[108:109], v[24:25]
	v_pk_fma_f32 v[12:13], v[12:13], v[110:111], v[26:27]
	s_waitcnt vmcnt(18)
	v_cvt_pk_bf16_f32 v28, v10, v11
	v_cvt_pk_bf16_f32 v29, v12, v13
	global_store_dwordx2 v[20:21], v[28:29], off
	v_add_co_u32_e32 v20, vcc, 0x10000, v20
	s_nop 1
	v_addc_co_u32_e32 v21, vcc, 0, v21, vcc
	v_lshlrev_b32_e32 v24, 16, v56
	v_and_b32_e32 v25, 0xffff0000, v56
	v_lshlrev_b32_e32 v26, 16, v57
	v_and_b32_e32 v27, 0xffff0000, v57
	v_pk_fma_f32 v[10:11], v[10:11], v[112:113], v[24:25]
	v_pk_fma_f32 v[12:13], v[12:13], v[114:115], v[26:27]
	s_waitcnt vmcnt(17)
	v_cvt_pk_bf16_f32 v28, v10, v11
	v_cvt_pk_bf16_f32 v29, v12, v13
	global_store_dwordx2 v[20:21], v[28:29], off
	v_add_co_u32_e32 v20, vcc, 0x10000, v20
	s_nop 1
	v_addc_co_u32_e32 v21, vcc, 0, v21, vcc
	v_lshlrev_b32_e32 v24, 16, v58
	v_and_b32_e32 v25, 0xffff0000, v58
	v_lshlrev_b32_e32 v26, 16, v59
	v_and_b32_e32 v27, 0xffff0000, v59
	v_pk_fma_f32 v[10:11], v[10:11], v[116:117], v[24:25]
	v_pk_fma_f32 v[12:13], v[12:13], v[118:119], v[26:27]
	s_waitcnt vmcnt(16)
	v_cvt_pk_bf16_f32 v28, v10, v11
	v_cvt_pk_bf16_f32 v29, v12, v13
	global_store_dwordx2 v[20:21], v[28:29], off
	v_add_co_u32_e32 v20, vcc, 0x10000, v20
	s_nop 1
	v_addc_co_u32_e32 v21, vcc, 0, v21, vcc
	v_lshlrev_b32_e32 v24, 16, v60
	v_and_b32_e32 v25, 0xffff0000, v60
	v_lshlrev_b32_e32 v26, 16, v61
	v_and_b32_e32 v27, 0xffff0000, v61
	v_pk_fma_f32 v[10:11], v[10:11], v[120:121], v[24:25]
	v_pk_fma_f32 v[12:13], v[12:13], v[122:123], v[26:27]
	s_waitcnt vmcnt(15)
	v_cvt_pk_bf16_f32 v28, v10, v11
	v_cvt_pk_bf16_f32 v29, v12, v13
	global_store_dwordx2 v[20:21], v[28:29], off
	v_add_co_u32_e32 v20, vcc, 0x10000, v20
	s_nop 1
	v_addc_co_u32_e32 v21, vcc, 0, v21, vcc
	v_lshlrev_b32_e32 v24, 16, v62
	v_and_b32_e32 v25, 0xffff0000, v62
	v_lshlrev_b32_e32 v26, 16, v63
	v_and_b32_e32 v27, 0xffff0000, v63
	v_pk_fma_f32 v[10:11], v[10:11], v[124:125], v[24:25]
	v_pk_fma_f32 v[12:13], v[12:13], v[126:127], v[26:27]
	global_load_dwordx2 v[32:33], v[18:19], off
	v_add_co_u32_e32 v18, vcc, 0x10000, v18
	s_nop 1
	v_addc_co_u32_e32 v19, vcc, 0, v19, vcc
	global_load_dwordx4 v[64:67], v[22:23], off
	global_load_dwordx2 v[34:35], v[18:19], off
	v_add_co_u32_e32 v18, vcc, 0x10000, v18
	s_nop 1
	v_addc_co_u32_e32 v19, vcc, 0, v19, vcc
	global_load_dwordx4 v[68:71], v[22:23], off offset:512
	global_load_dwordx2 v[36:37], v[18:19], off
	v_add_co_u32_e32 v18, vcc, 0x10000, v18
	s_nop 1
	v_addc_co_u32_e32 v19, vcc, 0, v19, vcc
	global_load_dwordx4 v[72:75], v[22:23], off offset:1024
	global_load_dwordx2 v[38:39], v[18:19], off
	v_add_co_u32_e32 v18, vcc, 0x10000, v18
	s_nop 1
	v_addc_co_u32_e32 v19, vcc, 0, v19, vcc
	global_load_dwordx4 v[76:79], v[22:23], off offset:1536
	global_load_dwordx2 v[40:41], v[18:19], off
	v_add_co_u32_e32 v18, vcc, 0x10000, v18
	s_nop 1
	v_addc_co_u32_e32 v19, vcc, 0, v19, vcc
	global_load_dwordx4 v[80:83], v[22:23], off offset:2048
	global_load_dwordx2 v[42:43], v[18:19], off
	v_add_co_u32_e32 v18, vcc, 0x10000, v18
	s_nop 1
	v_addc_co_u32_e32 v19, vcc, 0, v19, vcc
	global_load_dwordx4 v[84:87], v[22:23], off offset:2560
	global_load_dwordx2 v[44:45], v[18:19], off
	v_add_co_u32_e32 v18, vcc, 0x10000, v18
	s_nop 1
	v_addc_co_u32_e32 v19, vcc, 0, v19, vcc
	global_load_dwordx4 v[88:91], v[22:23], off offset:3072
	global_load_dwordx2 v[46:47], v[18:19], off
	v_add_co_u32_e32 v18, vcc, 0x10000, v18
	s_nop 1
	v_addc_co_u32_e32 v19, vcc, 0, v19, vcc
	global_load_dwordx4 v[92:95], v[22:23], off offset:3584
	v_add_co_u32_e32 v22, vcc, 0x1000, v22
	s_nop 1
	v_addc_co_u32_e32 v23, vcc, 0, v23, vcc
	global_load_dwordx2 v[48:49], v[18:19], off
	v_add_co_u32_e32 v18, vcc, 0x10000, v18
	s_nop 1
	v_addc_co_u32_e32 v19, vcc, 0, v19, vcc
	global_load_dwordx4 v[96:99], v[22:23], off
	global_load_dwordx2 v[50:51], v[18:19], off
	v_add_co_u32_e32 v18, vcc, 0x10000, v18
	s_nop 1
	v_addc_co_u32_e32 v19, vcc, 0, v19, vcc
	global_load_dwordx4 v[100:103], v[22:23], off offset:512
	global_load_dwordx2 v[52:53], v[18:19], off
	v_add_co_u32_e32 v18, vcc, 0x10000, v18
	s_nop 1
	v_addc_co_u32_e32 v19, vcc, 0, v19, vcc
	global_load_dwordx4 v[104:107], v[22:23], off offset:1024
	global_load_dwordx2 v[54:55], v[18:19], off
	v_add_co_u32_e32 v18, vcc, 0x10000, v18
	s_nop 1
	v_addc_co_u32_e32 v19, vcc, 0, v19, vcc
	global_load_dwordx4 v[108:111], v[22:23], off offset:1536
	global_load_dwordx2 v[56:57], v[18:19], off
	v_add_co_u32_e32 v18, vcc, 0x10000, v18
	s_nop 1
	v_addc_co_u32_e32 v19, vcc, 0, v19, vcc
	global_load_dwordx4 v[112:115], v[22:23], off offset:2048
	global_load_dwordx2 v[58:59], v[18:19], off
	v_add_co_u32_e32 v18, vcc, 0x10000, v18
	s_nop 1
	v_addc_co_u32_e32 v19, vcc, 0, v19, vcc
	global_load_dwordx4 v[116:119], v[22:23], off offset:2560
	global_load_dwordx2 v[60:61], v[18:19], off
	v_add_co_u32_e32 v18, vcc, 0x10000, v18
	s_nop 1
	v_addc_co_u32_e32 v19, vcc, 0, v19, vcc
	global_load_dwordx4 v[120:123], v[22:23], off offset:3072
	global_load_dwordx2 v[62:63], v[18:19], off
	v_add_co_u32_e32 v18, vcc, 0x10000, v18
	s_nop 1
	v_addc_co_u32_e32 v19, vcc, 0, v19, vcc
	global_load_dwordx4 v[124:127], v[22:23], off offset:3584
	v_add_co_u32_e32 v22, vcc, 0x1000, v22
	s_nop 1
	v_addc_co_u32_e32 v23, vcc, 0, v23, vcc
	s_waitcnt vmcnt(30)
	v_cvt_pk_bf16_f32 v28, v10, v11
	v_cvt_pk_bf16_f32 v29, v12, v13
	global_store_dwordx2 v[20:21], v[28:29], off
	v_add_co_u32_e32 v20, vcc, 0x10000, v20
	s_nop 1
	v_addc_co_u32_e32 v21, vcc, 0, v21, vcc
	v_lshlrev_b32_e32 v24, 16, v32
	v_and_b32_e32 v25, 0xffff0000, v32
	v_lshlrev_b32_e32 v26, 16, v33
	v_and_b32_e32 v27, 0xffff0000, v33
	v_pk_fma_f32 v[10:11], v[10:11], v[64:65], v[24:25]
	v_pk_fma_f32 v[12:13], v[12:13], v[66:67], v[26:27]
	s_waitcnt vmcnt(29)
	v_cvt_pk_bf16_f32 v28, v10, v11
	v_cvt_pk_bf16_f32 v29, v12, v13
	global_store_dwordx2 v[20:21], v[28:29], off
	v_add_co_u32_e32 v20, vcc, 0x10000, v20
	s_nop 1
	v_addc_co_u32_e32 v21, vcc, 0, v21, vcc
	v_lshlrev_b32_e32 v24, 16, v34
	v_and_b32_e32 v25, 0xffff0000, v34
	v_lshlrev_b32_e32 v26, 16, v35
	v_and_b32_e32 v27, 0xffff0000, v35
	v_pk_fma_f32 v[10:11], v[10:11], v[68:69], v[24:25]
	v_pk_fma_f32 v[12:13], v[12:13], v[70:71], v[26:27]
	s_waitcnt vmcnt(28)
	v_cvt_pk_bf16_f32 v28, v10, v11
	v_cvt_pk_bf16_f32 v29, v12, v13
	global_store_dwordx2 v[20:21], v[28:29], off
	v_add_co_u32_e32 v20, vcc, 0x10000, v20
	s_nop 1
	v_addc_co_u32_e32 v21, vcc, 0, v21, vcc
	v_lshlrev_b32_e32 v24, 16, v36
	v_and_b32_e32 v25, 0xffff0000, v36
	v_lshlrev_b32_e32 v26, 16, v37
	v_and_b32_e32 v27, 0xffff0000, v37
	v_pk_fma_f32 v[10:11], v[10:11], v[72:73], v[24:25]
	v_pk_fma_f32 v[12:13], v[12:13], v[74:75], v[26:27]
	s_waitcnt vmcnt(27)
	v_cvt_pk_bf16_f32 v28, v10, v11
	v_cvt_pk_bf16_f32 v29, v12, v13
	global_store_dwordx2 v[20:21], v[28:29], off
	v_add_co_u32_e32 v20, vcc, 0x10000, v20
	s_nop 1
	v_addc_co_u32_e32 v21, vcc, 0, v21, vcc
	v_lshlrev_b32_e32 v24, 16, v38
	v_and_b32_e32 v25, 0xffff0000, v38
	v_lshlrev_b32_e32 v26, 16, v39
	v_and_b32_e32 v27, 0xffff0000, v39
	v_pk_fma_f32 v[10:11], v[10:11], v[76:77], v[24:25]
	v_pk_fma_f32 v[12:13], v[12:13], v[78:79], v[26:27]
	s_waitcnt vmcnt(26)
	v_cvt_pk_bf16_f32 v28, v10, v11
	v_cvt_pk_bf16_f32 v29, v12, v13
	global_store_dwordx2 v[20:21], v[28:29], off
	v_add_co_u32_e32 v20, vcc, 0x10000, v20
	s_nop 1
	v_addc_co_u32_e32 v21, vcc, 0, v21, vcc
	v_lshlrev_b32_e32 v24, 16, v40
	v_and_b32_e32 v25, 0xffff0000, v40
	v_lshlrev_b32_e32 v26, 16, v41
	v_and_b32_e32 v27, 0xffff0000, v41
	v_pk_fma_f32 v[10:11], v[10:11], v[80:81], v[24:25]
	v_pk_fma_f32 v[12:13], v[12:13], v[82:83], v[26:27]
	s_waitcnt vmcnt(25)
	v_cvt_pk_bf16_f32 v28, v10, v11
	v_cvt_pk_bf16_f32 v29, v12, v13
	global_store_dwordx2 v[20:21], v[28:29], off
	v_add_co_u32_e32 v20, vcc, 0x10000, v20
	s_nop 1
	v_addc_co_u32_e32 v21, vcc, 0, v21, vcc
	v_lshlrev_b32_e32 v24, 16, v42
	v_and_b32_e32 v25, 0xffff0000, v42
	v_lshlrev_b32_e32 v26, 16, v43
	v_and_b32_e32 v27, 0xffff0000, v43
	v_pk_fma_f32 v[10:11], v[10:11], v[84:85], v[24:25]
	v_pk_fma_f32 v[12:13], v[12:13], v[86:87], v[26:27]
	s_waitcnt vmcnt(24)
	v_cvt_pk_bf16_f32 v28, v10, v11
	v_cvt_pk_bf16_f32 v29, v12, v13
	global_store_dwordx2 v[20:21], v[28:29], off
	v_add_co_u32_e32 v20, vcc, 0x10000, v20
	s_nop 1
	v_addc_co_u32_e32 v21, vcc, 0, v21, vcc
	v_lshlrev_b32_e32 v24, 16, v44
	v_and_b32_e32 v25, 0xffff0000, v44
	v_lshlrev_b32_e32 v26, 16, v45
	v_and_b32_e32 v27, 0xffff0000, v45
	v_pk_fma_f32 v[10:11], v[10:11], v[88:89], v[24:25]
	v_pk_fma_f32 v[12:13], v[12:13], v[90:91], v[26:27]
	s_waitcnt vmcnt(23)
	v_cvt_pk_bf16_f32 v28, v10, v11
	v_cvt_pk_bf16_f32 v29, v12, v13
	global_store_dwordx2 v[20:21], v[28:29], off
	v_add_co_u32_e32 v20, vcc, 0x10000, v20
	s_nop 1
	v_addc_co_u32_e32 v21, vcc, 0, v21, vcc
	v_lshlrev_b32_e32 v24, 16, v46
	v_and_b32_e32 v25, 0xffff0000, v46
	v_lshlrev_b32_e32 v26, 16, v47
	v_and_b32_e32 v27, 0xffff0000, v47
	v_pk_fma_f32 v[10:11], v[10:11], v[92:93], v[24:25]
	v_pk_fma_f32 v[12:13], v[12:13], v[94:95], v[26:27]
	s_waitcnt vmcnt(22)
	v_cvt_pk_bf16_f32 v28, v10, v11
	v_cvt_pk_bf16_f32 v29, v12, v13
	global_store_dwordx2 v[20:21], v[28:29], off
	v_add_co_u32_e32 v20, vcc, 0x10000, v20
	s_nop 1
	v_addc_co_u32_e32 v21, vcc, 0, v21, vcc
	v_lshlrev_b32_e32 v24, 16, v48
	v_and_b32_e32 v25, 0xffff0000, v48
	v_lshlrev_b32_e32 v26, 16, v49
	v_and_b32_e32 v27, 0xffff0000, v49
	v_pk_fma_f32 v[10:11], v[10:11], v[96:97], v[24:25]
	v_pk_fma_f32 v[12:13], v[12:13], v[98:99], v[26:27]
	s_waitcnt vmcnt(21)
	v_cvt_pk_bf16_f32 v28, v10, v11
	v_cvt_pk_bf16_f32 v29, v12, v13
	global_store_dwordx2 v[20:21], v[28:29], off
	v_add_co_u32_e32 v20, vcc, 0x10000, v20
	s_nop 1
	v_addc_co_u32_e32 v21, vcc, 0, v21, vcc
	v_lshlrev_b32_e32 v24, 16, v50
	v_and_b32_e32 v25, 0xffff0000, v50
	v_lshlrev_b32_e32 v26, 16, v51
	v_and_b32_e32 v27, 0xffff0000, v51
	v_pk_fma_f32 v[10:11], v[10:11], v[100:101], v[24:25]
	v_pk_fma_f32 v[12:13], v[12:13], v[102:103], v[26:27]
	s_waitcnt vmcnt(20)
	v_cvt_pk_bf16_f32 v28, v10, v11
	v_cvt_pk_bf16_f32 v29, v12, v13
	global_store_dwordx2 v[20:21], v[28:29], off
	v_add_co_u32_e32 v20, vcc, 0x10000, v20
	s_nop 1
	v_addc_co_u32_e32 v21, vcc, 0, v21, vcc
	v_lshlrev_b32_e32 v24, 16, v52
	v_and_b32_e32 v25, 0xffff0000, v52
	v_lshlrev_b32_e32 v26, 16, v53
	v_and_b32_e32 v27, 0xffff0000, v53
	v_pk_fma_f32 v[10:11], v[10:11], v[104:105], v[24:25]
	v_pk_fma_f32 v[12:13], v[12:13], v[106:107], v[26:27]
	s_waitcnt vmcnt(19)
	v_cvt_pk_bf16_f32 v28, v10, v11
	v_cvt_pk_bf16_f32 v29, v12, v13
	global_store_dwordx2 v[20:21], v[28:29], off
	v_add_co_u32_e32 v20, vcc, 0x10000, v20
	s_nop 1
	v_addc_co_u32_e32 v21, vcc, 0, v21, vcc
	v_lshlrev_b32_e32 v24, 16, v54
	v_and_b32_e32 v25, 0xffff0000, v54
	v_lshlrev_b32_e32 v26, 16, v55
	v_and_b32_e32 v27, 0xffff0000, v55
	v_pk_fma_f32 v[10:11], v[10:11], v[108:109], v[24:25]
	v_pk_fma_f32 v[12:13], v[12:13], v[110:111], v[26:27]
	s_waitcnt vmcnt(18)
	v_cvt_pk_bf16_f32 v28, v10, v11
	v_cvt_pk_bf16_f32 v29, v12, v13
	global_store_dwordx2 v[20:21], v[28:29], off
	v_add_co_u32_e32 v20, vcc, 0x10000, v20
	s_nop 1
	v_addc_co_u32_e32 v21, vcc, 0, v21, vcc
	v_lshlrev_b32_e32 v24, 16, v56
	v_and_b32_e32 v25, 0xffff0000, v56
	v_lshlrev_b32_e32 v26, 16, v57
	v_and_b32_e32 v27, 0xffff0000, v57
	v_pk_fma_f32 v[10:11], v[10:11], v[112:113], v[24:25]
	v_pk_fma_f32 v[12:13], v[12:13], v[114:115], v[26:27]
	s_waitcnt vmcnt(17)
	v_cvt_pk_bf16_f32 v28, v10, v11
	v_cvt_pk_bf16_f32 v29, v12, v13
	global_store_dwordx2 v[20:21], v[28:29], off
	v_add_co_u32_e32 v20, vcc, 0x10000, v20
	s_nop 1
	v_addc_co_u32_e32 v21, vcc, 0, v21, vcc
	v_lshlrev_b32_e32 v24, 16, v58
	v_and_b32_e32 v25, 0xffff0000, v58
	v_lshlrev_b32_e32 v26, 16, v59
	v_and_b32_e32 v27, 0xffff0000, v59
	v_pk_fma_f32 v[10:11], v[10:11], v[116:117], v[24:25]
	v_pk_fma_f32 v[12:13], v[12:13], v[118:119], v[26:27]
	s_waitcnt vmcnt(16)
	v_cvt_pk_bf16_f32 v28, v10, v11
	v_cvt_pk_bf16_f32 v29, v12, v13
	global_store_dwordx2 v[20:21], v[28:29], off
	v_add_co_u32_e32 v20, vcc, 0x10000, v20
	s_nop 1
	v_addc_co_u32_e32 v21, vcc, 0, v21, vcc
	v_lshlrev_b32_e32 v24, 16, v60
	v_and_b32_e32 v25, 0xffff0000, v60
	v_lshlrev_b32_e32 v26, 16, v61
	v_and_b32_e32 v27, 0xffff0000, v61
	v_pk_fma_f32 v[10:11], v[10:11], v[120:121], v[24:25]
	v_pk_fma_f32 v[12:13], v[12:13], v[122:123], v[26:27]
	s_waitcnt vmcnt(15)
	v_cvt_pk_bf16_f32 v28, v10, v11
	v_cvt_pk_bf16_f32 v29, v12, v13
	global_store_dwordx2 v[20:21], v[28:29], off
	v_add_co_u32_e32 v20, vcc, 0x10000, v20
	s_nop 1
	v_addc_co_u32_e32 v21, vcc, 0, v21, vcc
	v_lshlrev_b32_e32 v24, 16, v62
	v_and_b32_e32 v25, 0xffff0000, v62
	v_lshlrev_b32_e32 v26, 16, v63
	v_and_b32_e32 v27, 0xffff0000, v63
	v_pk_fma_f32 v[10:11], v[10:11], v[124:125], v[24:25]
	v_pk_fma_f32 v[12:13], v[12:13], v[126:127], v[26:27]
	v_readlane_b32 s12, v253, 44
	s_nop 1
	v_add_u32_e32 v16, s12, v16
	s_mov_b32 s12, 0x1ffff
	v_cmp_lt_i32_e32 vcc, s12, v16
	v_readlane_b32 s12, v254, 27
	s_or_b64 s[10:11], vcc, s[10:11]
	s_nop 0
	v_add_u32_e32 v15, s12, v15
	s_andn2_b64 exec, exec, s[10:11]
	s_cbranch_execnz .LBB0_457
	s_or_b64 exec, exec, s[10:11]
	s_mov_b64 s[10:11], 0

.LBB0_462:
	v_lshl_add_u64 v[18:19], s[8:9], 0, v[6:7]
	v_add_co_u32_e32 v18, vcc, 0x5e200000, v18
	s_nop 1
	v_addc_co_u32_e32 v19, vcc, 0, v19, vcc
	v_lshl_add_u64 v[22:23], s[8:9], 0, v[2:3]
	v_add_co_u32_e32 v22, vcc, 0x70480000, v22
	s_nop 1
	v_addc_co_u32_e32 v23, vcc, 0, v23, vcc
	v_mov_b32_e32 v20, v18
	v_mov_b32_e32 v21, v19
	v_add_co_u32_e32 v20, vcc, 0x4000000, v20
	s_nop 1
	v_addc_co_u32_e32 v21, vcc, 0, v21, vcc
	global_load_dwordx2 v[32:33], v[18:19], off
	v_add_co_u32_e32 v18, vcc, 0x40000, v18
	s_nop 1
	v_addc_co_u32_e32 v19, vcc, 0, v19, vcc
	global_load_dword v96, v[22:23], off offset:0
	global_load_dwordx2 v[34:35], v[18:19], off
	v_add_co_u32_e32 v18, vcc, 0x40000, v18
	s_nop 1
	v_addc_co_u32_e32 v19, vcc, 0, v19, vcc
	global_load_dword v97, v[22:23], off offset:64
	global_load_dwordx2 v[36:37], v[18:19], off
	v_add_co_u32_e32 v18, vcc, 0x40000, v18
	s_nop 1
	v_addc_co_u32_e32 v19, vcc, 0, v19, vcc
	global_load_dword v98, v[22:23], off offset:128
	global_load_dwordx2 v[38:39], v[18:19], off
	v_add_co_u32_e32 v18, vcc, 0x40000, v18
	s_nop 1
	v_addc_co_u32_e32 v19, vcc, 0, v19, vcc
	global_load_dword v99, v[22:23], off offset:192
	global_load_dwordx2 v[40:41], v[18:19], off
	v_add_co_u32_e32 v18, vcc, 0x40000, v18
	s_nop 1
	v_addc_co_u32_e32 v19, vcc, 0, v19, vcc
	global_load_dword v100, v[22:23], off offset:256
	global_load_dwordx2 v[42:43], v[18:19], off
	v_add_co_u32_e32 v18, vcc, 0x40000, v18
	s_nop 1
	v_addc_co_u32_e32 v19, vcc, 0, v19, vcc
	global_load_dword v101, v[22:23], off offset:320
	global_load_dwordx2 v[44:45], v[18:19], off
	v_add_co_u32_e32 v18, vcc, 0x40000, v18
	s_nop 1
	v_addc_co_u32_e32 v19, vcc, 0, v19, vcc
	global_load_dword v102, v[22:23], off offset:384
	global_load_dwordx2 v[46:47], v[18:19], off
	v_add_co_u32_e32 v18, vcc, 0x40000, v18
	s_nop 1
	v_addc_co_u32_e32 v19, vcc, 0, v19, vcc
	global_load_dword v103, v[22:23], off offset:448
	global_load_dwordx2 v[48:49], v[18:19], off
	v_add_co_u32_e32 v18, vcc, 0x40000, v18
	s_nop 1
	v_addc_co_u32_e32 v19, vcc, 0, v19, vcc
	global_load_dword v104, v[22:23], off offset:512
	global_load_dwordx2 v[50:51], v[18:19], off
	v_add_co_u32_e32 v18, vcc, 0x40000, v18
	s_nop 1
	v_addc_co_u32_e32 v19, vcc, 0, v19, vcc
	global_load_dword v105, v[22:23], off offset:576
	global_load_dwordx2 v[52:53], v[18:19], off
	v_add_co_u32_e32 v18, vcc, 0x40000, v18
	s_nop 1
	v_addc_co_u32_e32 v19, vcc, 0, v19, vcc
	global_load_dword v106, v[22:23], off offset:640
	global_load_dwordx2 v[54:55], v[18:19], off
	v_add_co_u32_e32 v18, vcc, 0x40000, v18
	s_nop 1
	v_addc_co_u32_e32 v19, vcc, 0, v19, vcc
	global_load_dword v107, v[22:23], off offset:704
	global_load_dwordx2 v[56:57], v[18:19], off
	v_add_co_u32_e32 v18, vcc, 0x40000, v18
	s_nop 1
	v_addc_co_u32_e32 v19, vcc, 0, v19, vcc
	global_load_dword v108, v[22:23], off offset:768
	global_load_dwordx2 v[58:59], v[18:19], off
	v_add_co_u32_e32 v18, vcc, 0x40000, v18
	s_nop 1
	v_addc_co_u32_e32 v19, vcc, 0, v19, vcc
	global_load_dword v109, v[22:23], off offset:832
	global_load_dwordx2 v[60:61], v[18:19], off
	v_add_co_u32_e32 v18, vcc, 0x40000, v18
	s_nop 1
	v_addc_co_u32_e32 v19, vcc, 0, v19, vcc
	global_load_dword v110, v[22:23], off offset:896
	global_load_dwordx2 v[62:63], v[18:19], off
	v_add_co_u32_e32 v18, vcc, 0x40000, v18
	s_nop 1
	v_addc_co_u32_e32 v19, vcc, 0, v19, vcc
	global_load_dword v111, v[22:23], off offset:960
	global_load_dwordx2 v[64:65], v[18:19], off
	v_add_co_u32_e32 v18, vcc, 0x40000, v18
	s_nop 1
	v_addc_co_u32_e32 v19, vcc, 0, v19, vcc
	global_load_dword v112, v[22:23], off offset:1024
	global_load_dwordx2 v[66:67], v[18:19], off
	v_add_co_u32_e32 v18, vcc, 0x40000, v18
	s_nop 1
	v_addc_co_u32_e32 v19, vcc, 0, v19, vcc
	global_load_dword v113, v[22:23], off offset:1088
	global_load_dwordx2 v[68:69], v[18:19], off
	v_add_co_u32_e32 v18, vcc, 0x40000, v18
	s_nop 1
	v_addc_co_u32_e32 v19, vcc, 0, v19, vcc
	global_load_dword v114, v[22:23], off offset:1152
	global_load_dwordx2 v[70:71], v[18:19], off
	v_add_co_u32_e32 v18, vcc, 0x40000, v18
	s_nop 1
	v_addc_co_u32_e32 v19, vcc, 0, v19, vcc
	global_load_dword v115, v[22:23], off offset:1216
	global_load_dwordx2 v[72:73], v[18:19], off
	v_add_co_u32_e32 v18, vcc, 0x40000, v18
	s_nop 1
	v_addc_co_u32_e32 v19, vcc, 0, v19, vcc
	global_load_dword v116, v[22:23], off offset:1280
	global_load_dwordx2 v[74:75], v[18:19], off
	v_add_co_u32_e32 v18, vcc, 0x40000, v18
	s_nop 1
	v_addc_co_u32_e32 v19, vcc, 0, v19, vcc
	global_load_dword v117, v[22:23], off offset:1344
	global_load_dwordx2 v[76:77], v[18:19], off
	v_add_co_u32_e32 v18, vcc, 0x40000, v18
	s_nop 1
	v_addc_co_u32_e32 v19, vcc, 0, v19, vcc
	global_load_dword v118, v[22:23], off offset:1408
	global_load_dwordx2 v[78:79], v[18:19], off
	v_add_co_u32_e32 v18, vcc, 0x40000, v18
	s_nop 1
	v_addc_co_u32_e32 v19, vcc, 0, v19, vcc
	global_load_dword v119, v[22:23], off offset:1472
	global_load_dwordx2 v[80:81], v[18:19], off
	v_add_co_u32_e32 v18, vcc, 0x40000, v18
	s_nop 1
	v_addc_co_u32_e32 v19, vcc, 0, v19, vcc
	global_load_dword v120, v[22:23], off offset:1536
	global_load_dwordx2 v[82:83], v[18:19], off
	v_add_co_u32_e32 v18, vcc, 0x40000, v18
	s_nop 1
	v_addc_co_u32_e32 v19, vcc, 0, v19, vcc
	global_load_dword v121, v[22:23], off offset:1600
	global_load_dwordx2 v[84:85], v[18:19], off
	v_add_co_u32_e32 v18, vcc, 0x40000, v18
	s_nop 1
	v_addc_co_u32_e32 v19, vcc, 0, v19, vcc
	global_load_dword v122, v[22:23], off offset:1664
	global_load_dwordx2 v[86:87], v[18:19], off
	v_add_co_u32_e32 v18, vcc, 0x40000, v18
	s_nop 1
	v_addc_co_u32_e32 v19, vcc, 0, v19, vcc
	global_load_dword v123, v[22:23], off offset:1728
	global_load_dwordx2 v[88:89], v[18:19], off
	v_add_co_u32_e32 v18, vcc, 0x40000, v18
	s_nop 1
	v_addc_co_u32_e32 v19, vcc, 0, v19, vcc
	global_load_dword v124, v[22:23], off offset:1792
	global_load_dwordx2 v[90:91], v[18:19], off
	v_add_co_u32_e32 v18, vcc, 0x40000, v18
	s_nop 1
	v_addc_co_u32_e32 v19, vcc, 0, v19, vcc
	global_load_dword v125, v[22:23], off offset:1856
	global_load_dwordx2 v[92:93], v[18:19], off
	v_add_co_u32_e32 v18, vcc, 0x40000, v18
	s_nop 1
	v_addc_co_u32_e32 v19, vcc, 0, v19, vcc
	global_load_dword v126, v[22:23], off offset:1920
	global_load_dwordx2 v[94:95], v[18:19], off
	v_add_co_u32_e32 v18, vcc, 0x40000, v18
	s_nop 1
	v_addc_co_u32_e32 v19, vcc, 0, v19, vcc
	global_load_dword v127, v[22:23], off offset:1984
	s_waitcnt vmcnt(62)
	v_cvt_pk_bf16_f32 v28, v10, v11
	v_cvt_pk_bf16_f32 v29, v12, v13
	global_store_dwordx2 v[20:21], v[28:29], off
	v_add_co_u32_e32 v20, vcc, 0x40000, v20
	s_nop 1
	v_addc_co_u32_e32 v21, vcc, 0, v21, vcc
	v_mul_f32_e32 v96, 0x3fb8aa3b, v96
	v_exp_f32_e32 v96, v96
	v_lshlrev_b32_e32 v24, 16, v32
	v_and_b32_e32 v25, 0xffff0000, v32
	v_lshlrev_b32_e32 v26, 16, v33
	v_and_b32_e32 v27, 0xffff0000, v33
	v_mov_b32_e32 v30, v96
	v_pk_fma_f32 v[10:11], v[10:11], v[30:31], v[24:25] op_sel_hi:[1,0,1]
	v_pk_fma_f32 v[12:13], v[12:13], v[30:31], v[26:27] op_sel_hi:[1,0,1]
	s_waitcnt vmcnt(61)
	v_cvt_pk_bf16_f32 v28, v10, v11
	v_cvt_pk_bf16_f32 v29, v12, v13
	global_store_dwordx2 v[20:21], v[28:29], off
	v_add_co_u32_e32 v20, vcc, 0x40000, v20
	s_nop 1
	v_addc_co_u32_e32 v21, vcc, 0, v21, vcc
	v_mul_f32_e32 v97, 0x3fb8aa3b, v97
	v_exp_f32_e32 v97, v97
	v_lshlrev_b32_e32 v24, 16, v34
	v_and_b32_e32 v25, 0xffff0000, v34
	v_lshlrev_b32_e32 v26, 16, v35
	v_and_b32_e32 v27, 0xffff0000, v35
	v_mov_b32_e32 v30, v97
	v_pk_fma_f32 v[10:11], v[10:11], v[30:31], v[24:25] op_sel_hi:[1,0,1]
	v_pk_fma_f32 v[12:13], v[12:13], v[30:31], v[26:27] op_sel_hi:[1,0,1]
	s_waitcnt vmcnt(60)
	v_cvt_pk_bf16_f32 v28, v10, v11
	v_cvt_pk_bf16_f32 v29, v12, v13
	global_store_dwordx2 v[20:21], v[28:29], off
	v_add_co_u32_e32 v20, vcc, 0x40000, v20
	s_nop 1
	v_addc_co_u32_e32 v21, vcc, 0, v21, vcc
	v_mul_f32_e32 v98, 0x3fb8aa3b, v98
	v_exp_f32_e32 v98, v98
	v_lshlrev_b32_e32 v24, 16, v36
	v_and_b32_e32 v25, 0xffff0000, v36
	v_lshlrev_b32_e32 v26, 16, v37
	v_and_b32_e32 v27, 0xffff0000, v37
	v_mov_b32_e32 v30, v98
	v_pk_fma_f32 v[10:11], v[10:11], v[30:31], v[24:25] op_sel_hi:[1,0,1]
	v_pk_fma_f32 v[12:13], v[12:13], v[30:31], v[26:27] op_sel_hi:[1,0,1]
	s_waitcnt vmcnt(59)
	v_cvt_pk_bf16_f32 v28, v10, v11
	v_cvt_pk_bf16_f32 v29, v12, v13
	global_store_dwordx2 v[20:21], v[28:29], off
	v_add_co_u32_e32 v20, vcc, 0x40000, v20
	s_nop 1
	v_addc_co_u32_e32 v21, vcc, 0, v21, vcc
	v_mul_f32_e32 v99, 0x3fb8aa3b, v99
	v_exp_f32_e32 v99, v99
	v_lshlrev_b32_e32 v24, 16, v38
	v_and_b32_e32 v25, 0xffff0000, v38
	v_lshlrev_b32_e32 v26, 16, v39
	v_and_b32_e32 v27, 0xffff0000, v39
	v_mov_b32_e32 v30, v99
	v_pk_fma_f32 v[10:11], v[10:11], v[30:31], v[24:25] op_sel_hi:[1,0,1]
	v_pk_fma_f32 v[12:13], v[12:13], v[30:31], v[26:27] op_sel_hi:[1,0,1]
	s_waitcnt vmcnt(58)
	v_cvt_pk_bf16_f32 v28, v10, v11
	v_cvt_pk_bf16_f32 v29, v12, v13
	global_store_dwordx2 v[20:21], v[28:29], off
	v_add_co_u32_e32 v20, vcc, 0x40000, v20
	s_nop 1
	v_addc_co_u32_e32 v21, vcc, 0, v21, vcc
	v_mul_f32_e32 v100, 0x3fb8aa3b, v100
	v_exp_f32_e32 v100, v100
	v_lshlrev_b32_e32 v24, 16, v40
	v_and_b32_e32 v25, 0xffff0000, v40
	v_lshlrev_b32_e32 v26, 16, v41
	v_and_b32_e32 v27, 0xffff0000, v41
	v_mov_b32_e32 v30, v100
	v_pk_fma_f32 v[10:11], v[10:11], v[30:31], v[24:25] op_sel_hi:[1,0,1]
	v_pk_fma_f32 v[12:13], v[12:13], v[30:31], v[26:27] op_sel_hi:[1,0,1]
	s_waitcnt vmcnt(57)
	v_cvt_pk_bf16_f32 v28, v10, v11
	v_cvt_pk_bf16_f32 v29, v12, v13
	global_store_dwordx2 v[20:21], v[28:29], off
	v_add_co_u32_e32 v20, vcc, 0x40000, v20
	s_nop 1
	v_addc_co_u32_e32 v21, vcc, 0, v21, vcc
	v_mul_f32_e32 v101, 0x3fb8aa3b, v101
	v_exp_f32_e32 v101, v101
	v_lshlrev_b32_e32 v24, 16, v42
	v_and_b32_e32 v25, 0xffff0000, v42
	v_lshlrev_b32_e32 v26, 16, v43
	v_and_b32_e32 v27, 0xffff0000, v43
	v_mov_b32_e32 v30, v101
	v_pk_fma_f32 v[10:11], v[10:11], v[30:31], v[24:25] op_sel_hi:[1,0,1]
	v_pk_fma_f32 v[12:13], v[12:13], v[30:31], v[26:27] op_sel_hi:[1,0,1]
	s_waitcnt vmcnt(56)
	v_cvt_pk_bf16_f32 v28, v10, v11
	v_cvt_pk_bf16_f32 v29, v12, v13
	global_store_dwordx2 v[20:21], v[28:29], off
	v_add_co_u32_e32 v20, vcc, 0x40000, v20
	s_nop 1
	v_addc_co_u32_e32 v21, vcc, 0, v21, vcc
	v_mul_f32_e32 v102, 0x3fb8aa3b, v102
	v_exp_f32_e32 v102, v102
	v_lshlrev_b32_e32 v24, 16, v44
	v_and_b32_e32 v25, 0xffff0000, v44
	v_lshlrev_b32_e32 v26, 16, v45
	v_and_b32_e32 v27, 0xffff0000, v45
	v_mov_b32_e32 v30, v102
	v_pk_fma_f32 v[10:11], v[10:11], v[30:31], v[24:25] op_sel_hi:[1,0,1]
	v_pk_fma_f32 v[12:13], v[12:13], v[30:31], v[26:27] op_sel_hi:[1,0,1]
	s_waitcnt vmcnt(55)
	v_cvt_pk_bf16_f32 v28, v10, v11
	v_cvt_pk_bf16_f32 v29, v12, v13
	global_store_dwordx2 v[20:21], v[28:29], off
	v_add_co_u32_e32 v20, vcc, 0x40000, v20
	s_nop 1
	v_addc_co_u32_e32 v21, vcc, 0, v21, vcc
	v_mul_f32_e32 v103, 0x3fb8aa3b, v103
	v_exp_f32_e32 v103, v103
	v_lshlrev_b32_e32 v24, 16, v46
	v_and_b32_e32 v25, 0xffff0000, v46
	v_lshlrev_b32_e32 v26, 16, v47
	v_and_b32_e32 v27, 0xffff0000, v47
	v_mov_b32_e32 v30, v103
	v_pk_fma_f32 v[10:11], v[10:11], v[30:31], v[24:25] op_sel_hi:[1,0,1]
	v_pk_fma_f32 v[12:13], v[12:13], v[30:31], v[26:27] op_sel_hi:[1,0,1]
	s_waitcnt vmcnt(54)
	v_cvt_pk_bf16_f32 v28, v10, v11
	v_cvt_pk_bf16_f32 v29, v12, v13
	global_store_dwordx2 v[20:21], v[28:29], off
	v_add_co_u32_e32 v20, vcc, 0x40000, v20
	s_nop 1
	v_addc_co_u32_e32 v21, vcc, 0, v21, vcc
	v_mul_f32_e32 v104, 0x3fb8aa3b, v104
	v_exp_f32_e32 v104, v104
	v_lshlrev_b32_e32 v24, 16, v48
	v_and_b32_e32 v25, 0xffff0000, v48
	v_lshlrev_b32_e32 v26, 16, v49
	v_and_b32_e32 v27, 0xffff0000, v49
	v_mov_b32_e32 v30, v104
	v_pk_fma_f32 v[10:11], v[10:11], v[30:31], v[24:25] op_sel_hi:[1,0,1]
	v_pk_fma_f32 v[12:13], v[12:13], v[30:31], v[26:27] op_sel_hi:[1,0,1]
	s_waitcnt vmcnt(53)
	v_cvt_pk_bf16_f32 v28, v10, v11
	v_cvt_pk_bf16_f32 v29, v12, v13
	global_store_dwordx2 v[20:21], v[28:29], off
	v_add_co_u32_e32 v20, vcc, 0x40000, v20
	s_nop 1
	v_addc_co_u32_e32 v21, vcc, 0, v21, vcc
	v_mul_f32_e32 v105, 0x3fb8aa3b, v105
	v_exp_f32_e32 v105, v105
	v_lshlrev_b32_e32 v24, 16, v50
	v_and_b32_e32 v25, 0xffff0000, v50
	v_lshlrev_b32_e32 v26, 16, v51
	v_and_b32_e32 v27, 0xffff0000, v51
	v_mov_b32_e32 v30, v105
	v_pk_fma_f32 v[10:11], v[10:11], v[30:31], v[24:25] op_sel_hi:[1,0,1]
	v_pk_fma_f32 v[12:13], v[12:13], v[30:31], v[26:27] op_sel_hi:[1,0,1]
	s_waitcnt vmcnt(52)
	v_cvt_pk_bf16_f32 v28, v10, v11
	v_cvt_pk_bf16_f32 v29, v12, v13
	global_store_dwordx2 v[20:21], v[28:29], off
	v_add_co_u32_e32 v20, vcc, 0x40000, v20
	s_nop 1
	v_addc_co_u32_e32 v21, vcc, 0, v21, vcc
	v_mul_f32_e32 v106, 0x3fb8aa3b, v106
	v_exp_f32_e32 v106, v106
	v_lshlrev_b32_e32 v24, 16, v52
	v_and_b32_e32 v25, 0xffff0000, v52
	v_lshlrev_b32_e32 v26, 16, v53
	v_and_b32_e32 v27, 0xffff0000, v53
	v_mov_b32_e32 v30, v106
	v_pk_fma_f32 v[10:11], v[10:11], v[30:31], v[24:25] op_sel_hi:[1,0,1]
	v_pk_fma_f32 v[12:13], v[12:13], v[30:31], v[26:27] op_sel_hi:[1,0,1]
	s_waitcnt vmcnt(51)
	v_cvt_pk_bf16_f32 v28, v10, v11
	v_cvt_pk_bf16_f32 v29, v12, v13
	global_store_dwordx2 v[20:21], v[28:29], off
	v_add_co_u32_e32 v20, vcc, 0x40000, v20
	s_nop 1
	v_addc_co_u32_e32 v21, vcc, 0, v21, vcc
	v_mul_f32_e32 v107, 0x3fb8aa3b, v107
	v_exp_f32_e32 v107, v107
	v_lshlrev_b32_e32 v24, 16, v54
	v_and_b32_e32 v25, 0xffff0000, v54
	v_lshlrev_b32_e32 v26, 16, v55
	v_and_b32_e32 v27, 0xffff0000, v55
	v_mov_b32_e32 v30, v107
	v_pk_fma_f32 v[10:11], v[10:11], v[30:31], v[24:25] op_sel_hi:[1,0,1]
	v_pk_fma_f32 v[12:13], v[12:13], v[30:31], v[26:27] op_sel_hi:[1,0,1]
	s_waitcnt vmcnt(50)
	v_cvt_pk_bf16_f32 v28, v10, v11
	v_cvt_pk_bf16_f32 v29, v12, v13
	global_store_dwordx2 v[20:21], v[28:29], off
	v_add_co_u32_e32 v20, vcc, 0x40000, v20
	s_nop 1
	v_addc_co_u32_e32 v21, vcc, 0, v21, vcc
	v_mul_f32_e32 v108, 0x3fb8aa3b, v108
	v_exp_f32_e32 v108, v108
	v_lshlrev_b32_e32 v24, 16, v56
	v_and_b32_e32 v25, 0xffff0000, v56
	v_lshlrev_b32_e32 v26, 16, v57
	v_and_b32_e32 v27, 0xffff0000, v57
	v_mov_b32_e32 v30, v108
	v_pk_fma_f32 v[10:11], v[10:11], v[30:31], v[24:25] op_sel_hi:[1,0,1]
	v_pk_fma_f32 v[12:13], v[12:13], v[30:31], v[26:27] op_sel_hi:[1,0,1]
	s_waitcnt vmcnt(49)
	v_cvt_pk_bf16_f32 v28, v10, v11
	v_cvt_pk_bf16_f32 v29, v12, v13
	global_store_dwordx2 v[20:21], v[28:29], off
	v_add_co_u32_e32 v20, vcc, 0x40000, v20
	s_nop 1
	v_addc_co_u32_e32 v21, vcc, 0, v21, vcc
	v_mul_f32_e32 v109, 0x3fb8aa3b, v109
	v_exp_f32_e32 v109, v109
	v_lshlrev_b32_e32 v24, 16, v58
	v_and_b32_e32 v25, 0xffff0000, v58
	v_lshlrev_b32_e32 v26, 16, v59
	v_and_b32_e32 v27, 0xffff0000, v59
	v_mov_b32_e32 v30, v109
	v_pk_fma_f32 v[10:11], v[10:11], v[30:31], v[24:25] op_sel_hi:[1,0,1]
	v_pk_fma_f32 v[12:13], v[12:13], v[30:31], v[26:27] op_sel_hi:[1,0,1]
	s_waitcnt vmcnt(48)
	v_cvt_pk_bf16_f32 v28, v10, v11
	v_cvt_pk_bf16_f32 v29, v12, v13
	global_store_dwordx2 v[20:21], v[28:29], off
	v_add_co_u32_e32 v20, vcc, 0x40000, v20
	s_nop 1
	v_addc_co_u32_e32 v21, vcc, 0, v21, vcc
	v_mul_f32_e32 v110, 0x3fb8aa3b, v110
	v_exp_f32_e32 v110, v110
	v_lshlrev_b32_e32 v24, 16, v60
	v_and_b32_e32 v25, 0xffff0000, v60
	v_lshlrev_b32_e32 v26, 16, v61
	v_and_b32_e32 v27, 0xffff0000, v61
	v_mov_b32_e32 v30, v110
	v_pk_fma_f32 v[10:11], v[10:11], v[30:31], v[24:25] op_sel_hi:[1,0,1]
	v_pk_fma_f32 v[12:13], v[12:13], v[30:31], v[26:27] op_sel_hi:[1,0,1]
	s_waitcnt vmcnt(47)
	v_cvt_pk_bf16_f32 v28, v10, v11
	v_cvt_pk_bf16_f32 v29, v12, v13
	global_store_dwordx2 v[20:21], v[28:29], off
	v_add_co_u32_e32 v20, vcc, 0x40000, v20
	s_nop 1
	v_addc_co_u32_e32 v21, vcc, 0, v21, vcc
	v_mul_f32_e32 v111, 0x3fb8aa3b, v111
	v_exp_f32_e32 v111, v111
	v_lshlrev_b32_e32 v24, 16, v62
	v_and_b32_e32 v25, 0xffff0000, v62
	v_lshlrev_b32_e32 v26, 16, v63
	v_and_b32_e32 v27, 0xffff0000, v63
	v_mov_b32_e32 v30, v111
	v_pk_fma_f32 v[10:11], v[10:11], v[30:31], v[24:25] op_sel_hi:[1,0,1]
	v_pk_fma_f32 v[12:13], v[12:13], v[30:31], v[26:27] op_sel_hi:[1,0,1]
	s_waitcnt vmcnt(46)
	v_cvt_pk_bf16_f32 v28, v10, v11
	v_cvt_pk_bf16_f32 v29, v12, v13
	global_store_dwordx2 v[20:21], v[28:29], off
	v_add_co_u32_e32 v20, vcc, 0x40000, v20
	s_nop 1
	v_addc_co_u32_e32 v21, vcc, 0, v21, vcc
	v_mul_f32_e32 v112, 0x3fb8aa3b, v112
	v_exp_f32_e32 v112, v112
	v_lshlrev_b32_e32 v24, 16, v64
	v_and_b32_e32 v25, 0xffff0000, v64
	v_lshlrev_b32_e32 v26, 16, v65
	v_and_b32_e32 v27, 0xffff0000, v65
	v_mov_b32_e32 v30, v112
	v_pk_fma_f32 v[10:11], v[10:11], v[30:31], v[24:25] op_sel_hi:[1,0,1]
	v_pk_fma_f32 v[12:13], v[12:13], v[30:31], v[26:27] op_sel_hi:[1,0,1]
	s_waitcnt vmcnt(45)
	v_cvt_pk_bf16_f32 v28, v10, v11
	v_cvt_pk_bf16_f32 v29, v12, v13
	global_store_dwordx2 v[20:21], v[28:29], off
	v_add_co_u32_e32 v20, vcc, 0x40000, v20
	s_nop 1
	v_addc_co_u32_e32 v21, vcc, 0, v21, vcc
	v_mul_f32_e32 v113, 0x3fb8aa3b, v113
	v_exp_f32_e32 v113, v113
	v_lshlrev_b32_e32 v24, 16, v66
	v_and_b32_e32 v25, 0xffff0000, v66
	v_lshlrev_b32_e32 v26, 16, v67
	v_and_b32_e32 v27, 0xffff0000, v67
	v_mov_b32_e32 v30, v113
	v_pk_fma_f32 v[10:11], v[10:11], v[30:31], v[24:25] op_sel_hi:[1,0,1]
	v_pk_fma_f32 v[12:13], v[12:13], v[30:31], v[26:27] op_sel_hi:[1,0,1]
	s_waitcnt vmcnt(44)
	v_cvt_pk_bf16_f32 v28, v10, v11
	v_cvt_pk_bf16_f32 v29, v12, v13
	global_store_dwordx2 v[20:21], v[28:29], off
	v_add_co_u32_e32 v20, vcc, 0x40000, v20
	s_nop 1
	v_addc_co_u32_e32 v21, vcc, 0, v21, vcc
	v_mul_f32_e32 v114, 0x3fb8aa3b, v114
	v_exp_f32_e32 v114, v114
	v_lshlrev_b32_e32 v24, 16, v68
	v_and_b32_e32 v25, 0xffff0000, v68
	v_lshlrev_b32_e32 v26, 16, v69
	v_and_b32_e32 v27, 0xffff0000, v69
	v_mov_b32_e32 v30, v114
	v_pk_fma_f32 v[10:11], v[10:11], v[30:31], v[24:25] op_sel_hi:[1,0,1]
	v_pk_fma_f32 v[12:13], v[12:13], v[30:31], v[26:27] op_sel_hi:[1,0,1]
	s_waitcnt vmcnt(43)
	v_cvt_pk_bf16_f32 v28, v10, v11
	v_cvt_pk_bf16_f32 v29, v12, v13
	global_store_dwordx2 v[20:21], v[28:29], off
	v_add_co_u32_e32 v20, vcc, 0x40000, v20
	s_nop 1
	v_addc_co_u32_e32 v21, vcc, 0, v21, vcc
	v_mul_f32_e32 v115, 0x3fb8aa3b, v115
	v_exp_f32_e32 v115, v115
	v_lshlrev_b32_e32 v24, 16, v70
	v_and_b32_e32 v25, 0xffff0000, v70
	v_lshlrev_b32_e32 v26, 16, v71
	v_and_b32_e32 v27, 0xffff0000, v71
	v_mov_b32_e32 v30, v115
	v_pk_fma_f32 v[10:11], v[10:11], v[30:31], v[24:25] op_sel_hi:[1,0,1]
	v_pk_fma_f32 v[12:13], v[12:13], v[30:31], v[26:27] op_sel_hi:[1,0,1]
	s_waitcnt vmcnt(42)
	v_cvt_pk_bf16_f32 v28, v10, v11
	v_cvt_pk_bf16_f32 v29, v12, v13
	global_store_dwordx2 v[20:21], v[28:29], off
	v_add_co_u32_e32 v20, vcc, 0x40000, v20
	s_nop 1
	v_addc_co_u32_e32 v21, vcc, 0, v21, vcc
	v_mul_f32_e32 v116, 0x3fb8aa3b, v116
	v_exp_f32_e32 v116, v116
	v_lshlrev_b32_e32 v24, 16, v72
	v_and_b32_e32 v25, 0xffff0000, v72
	v_lshlrev_b32_e32 v26, 16, v73
	v_and_b32_e32 v27, 0xffff0000, v73
	v_mov_b32_e32 v30, v116
	v_pk_fma_f32 v[10:11], v[10:11], v[30:31], v[24:25] op_sel_hi:[1,0,1]
	v_pk_fma_f32 v[12:13], v[12:13], v[30:31], v[26:27] op_sel_hi:[1,0,1]
	s_waitcnt vmcnt(41)
	v_cvt_pk_bf16_f32 v28, v10, v11
	v_cvt_pk_bf16_f32 v29, v12, v13
	global_store_dwordx2 v[20:21], v[28:29], off
	v_add_co_u32_e32 v20, vcc, 0x40000, v20
	s_nop 1
	v_addc_co_u32_e32 v21, vcc, 0, v21, vcc
	v_mul_f32_e32 v117, 0x3fb8aa3b, v117
	v_exp_f32_e32 v117, v117
	v_lshlrev_b32_e32 v24, 16, v74
	v_and_b32_e32 v25, 0xffff0000, v74
	v_lshlrev_b32_e32 v26, 16, v75
	v_and_b32_e32 v27, 0xffff0000, v75
	v_mov_b32_e32 v30, v117
	v_pk_fma_f32 v[10:11], v[10:11], v[30:31], v[24:25] op_sel_hi:[1,0,1]
	v_pk_fma_f32 v[12:13], v[12:13], v[30:31], v[26:27] op_sel_hi:[1,0,1]
	s_waitcnt vmcnt(40)
	v_cvt_pk_bf16_f32 v28, v10, v11
	v_cvt_pk_bf16_f32 v29, v12, v13
	global_store_dwordx2 v[20:21], v[28:29], off
	v_add_co_u32_e32 v20, vcc, 0x40000, v20
	s_nop 1
	v_addc_co_u32_e32 v21, vcc, 0, v21, vcc
	v_mul_f32_e32 v118, 0x3fb8aa3b, v118
	v_exp_f32_e32 v118, v118
	v_lshlrev_b32_e32 v24, 16, v76
	v_and_b32_e32 v25, 0xffff0000, v76
	v_lshlrev_b32_e32 v26, 16, v77
	v_and_b32_e32 v27, 0xffff0000, v77
	v_mov_b32_e32 v30, v118
	v_pk_fma_f32 v[10:11], v[10:11], v[30:31], v[24:25] op_sel_hi:[1,0,1]
	v_pk_fma_f32 v[12:13], v[12:13], v[30:31], v[26:27] op_sel_hi:[1,0,1]
	s_waitcnt vmcnt(39)
	v_cvt_pk_bf16_f32 v28, v10, v11
	v_cvt_pk_bf16_f32 v29, v12, v13
	global_store_dwordx2 v[20:21], v[28:29], off
	v_add_co_u32_e32 v20, vcc, 0x40000, v20
	s_nop 1
	v_addc_co_u32_e32 v21, vcc, 0, v21, vcc
	v_mul_f32_e32 v119, 0x3fb8aa3b, v119
	v_exp_f32_e32 v119, v119
	v_lshlrev_b32_e32 v24, 16, v78
	v_and_b32_e32 v25, 0xffff0000, v78
	v_lshlrev_b32_e32 v26, 16, v79
	v_and_b32_e32 v27, 0xffff0000, v79
	v_mov_b32_e32 v30, v119
	v_pk_fma_f32 v[10:11], v[10:11], v[30:31], v[24:25] op_sel_hi:[1,0,1]
	v_pk_fma_f32 v[12:13], v[12:13], v[30:31], v[26:27] op_sel_hi:[1,0,1]
	s_waitcnt vmcnt(38)
	v_cvt_pk_bf16_f32 v28, v10, v11
	v_cvt_pk_bf16_f32 v29, v12, v13
	global_store_dwordx2 v[20:21], v[28:29], off
	v_add_co_u32_e32 v20, vcc, 0x40000, v20
	s_nop 1
	v_addc_co_u32_e32 v21, vcc, 0, v21, vcc
	v_mul_f32_e32 v120, 0x3fb8aa3b, v120
	v_exp_f32_e32 v120, v120
	v_lshlrev_b32_e32 v24, 16, v80
	v_and_b32_e32 v25, 0xffff0000, v80
	v_lshlrev_b32_e32 v26, 16, v81
	v_and_b32_e32 v27, 0xffff0000, v81
	v_mov_b32_e32 v30, v120
	v_pk_fma_f32 v[10:11], v[10:11], v[30:31], v[24:25] op_sel_hi:[1,0,1]
	v_pk_fma_f32 v[12:13], v[12:13], v[30:31], v[26:27] op_sel_hi:[1,0,1]
	s_waitcnt vmcnt(37)
	v_cvt_pk_bf16_f32 v28, v10, v11
	v_cvt_pk_bf16_f32 v29, v12, v13
	global_store_dwordx2 v[20:21], v[28:29], off
	v_add_co_u32_e32 v20, vcc, 0x40000, v20
	s_nop 1
	v_addc_co_u32_e32 v21, vcc, 0, v21, vcc
	v_mul_f32_e32 v121, 0x3fb8aa3b, v121
	v_exp_f32_e32 v121, v121
	v_lshlrev_b32_e32 v24, 16, v82
	v_and_b32_e32 v25, 0xffff0000, v82
	v_lshlrev_b32_e32 v26, 16, v83
	v_and_b32_e32 v27, 0xffff0000, v83
	v_mov_b32_e32 v30, v121
	v_pk_fma_f32 v[10:11], v[10:11], v[30:31], v[24:25] op_sel_hi:[1,0,1]
	v_pk_fma_f32 v[12:13], v[12:13], v[30:31], v[26:27] op_sel_hi:[1,0,1]
	s_waitcnt vmcnt(36)
	v_cvt_pk_bf16_f32 v28, v10, v11
	v_cvt_pk_bf16_f32 v29, v12, v13
	global_store_dwordx2 v[20:21], v[28:29], off
	v_add_co_u32_e32 v20, vcc, 0x40000, v20
	s_nop 1
	v_addc_co_u32_e32 v21, vcc, 0, v21, vcc
	v_mul_f32_e32 v122, 0x3fb8aa3b, v122
	v_exp_f32_e32 v122, v122
	v_lshlrev_b32_e32 v24, 16, v84
	v_and_b32_e32 v25, 0xffff0000, v84
	v_lshlrev_b32_e32 v26, 16, v85
	v_and_b32_e32 v27, 0xffff0000, v85
	v_mov_b32_e32 v30, v122
	v_pk_fma_f32 v[10:11], v[10:11], v[30:31], v[24:25] op_sel_hi:[1,0,1]
	v_pk_fma_f32 v[12:13], v[12:13], v[30:31], v[26:27] op_sel_hi:[1,0,1]
	s_waitcnt vmcnt(35)
	v_cvt_pk_bf16_f32 v28, v10, v11
	v_cvt_pk_bf16_f32 v29, v12, v13
	global_store_dwordx2 v[20:21], v[28:29], off
	v_add_co_u32_e32 v20, vcc, 0x40000, v20
	s_nop 1
	v_addc_co_u32_e32 v21, vcc, 0, v21, vcc
	v_mul_f32_e32 v123, 0x3fb8aa3b, v123
	v_exp_f32_e32 v123, v123
	v_lshlrev_b32_e32 v24, 16, v86
	v_and_b32_e32 v25, 0xffff0000, v86
	v_lshlrev_b32_e32 v26, 16, v87
	v_and_b32_e32 v27, 0xffff0000, v87
	v_mov_b32_e32 v30, v123
	v_pk_fma_f32 v[10:11], v[10:11], v[30:31], v[24:25] op_sel_hi:[1,0,1]
	v_pk_fma_f32 v[12:13], v[12:13], v[30:31], v[26:27] op_sel_hi:[1,0,1]
	s_waitcnt vmcnt(34)
	v_cvt_pk_bf16_f32 v28, v10, v11
	v_cvt_pk_bf16_f32 v29, v12, v13
	global_store_dwordx2 v[20:21], v[28:29], off
	v_add_co_u32_e32 v20, vcc, 0x40000, v20
	s_nop 1
	v_addc_co_u32_e32 v21, vcc, 0, v21, vcc
	v_mul_f32_e32 v124, 0x3fb8aa3b, v124
	v_exp_f32_e32 v124, v124
	v_lshlrev_b32_e32 v24, 16, v88
	v_and_b32_e32 v25, 0xffff0000, v88
	v_lshlrev_b32_e32 v26, 16, v89
	v_and_b32_e32 v27, 0xffff0000, v89
	v_mov_b32_e32 v30, v124
	v_pk_fma_f32 v[10:11], v[10:11], v[30:31], v[24:25] op_sel_hi:[1,0,1]
	v_pk_fma_f32 v[12:13], v[12:13], v[30:31], v[26:27] op_sel_hi:[1,0,1]
	s_waitcnt vmcnt(33)
	v_cvt_pk_bf16_f32 v28, v10, v11
	v_cvt_pk_bf16_f32 v29, v12, v13
	global_store_dwordx2 v[20:21], v[28:29], off
	v_add_co_u32_e32 v20, vcc, 0x40000, v20
	s_nop 1
	v_addc_co_u32_e32 v21, vcc, 0, v21, vcc
	v_mul_f32_e32 v125, 0x3fb8aa3b, v125
	v_exp_f32_e32 v125, v125
	v_lshlrev_b32_e32 v24, 16, v90
	v_and_b32_e32 v25, 0xffff0000, v90
	v_lshlrev_b32_e32 v26, 16, v91
	v_and_b32_e32 v27, 0xffff0000, v91
	v_mov_b32_e32 v30, v125
	v_pk_fma_f32 v[10:11], v[10:11], v[30:31], v[24:25] op_sel_hi:[1,0,1]
	v_pk_fma_f32 v[12:13], v[12:13], v[30:31], v[26:27] op_sel_hi:[1,0,1]
	s_waitcnt vmcnt(32)
	v_cvt_pk_bf16_f32 v28, v10, v11
	v_cvt_pk_bf16_f32 v29, v12, v13
	global_store_dwordx2 v[20:21], v[28:29], off
	v_add_co_u32_e32 v20, vcc, 0x40000, v20
	s_nop 1
	v_addc_co_u32_e32 v21, vcc, 0, v21, vcc
	v_mul_f32_e32 v126, 0x3fb8aa3b, v126
	v_exp_f32_e32 v126, v126
	v_lshlrev_b32_e32 v24, 16, v92
	v_and_b32_e32 v25, 0xffff0000, v92
	v_lshlrev_b32_e32 v26, 16, v93
	v_and_b32_e32 v27, 0xffff0000, v93
	v_mov_b32_e32 v30, v126
	v_pk_fma_f32 v[10:11], v[10:11], v[30:31], v[24:25] op_sel_hi:[1,0,1]
	v_pk_fma_f32 v[12:13], v[12:13], v[30:31], v[26:27] op_sel_hi:[1,0,1]
	s_waitcnt vmcnt(31)
	v_cvt_pk_bf16_f32 v28, v10, v11
	v_cvt_pk_bf16_f32 v29, v12, v13
	global_store_dwordx2 v[20:21], v[28:29], off
	v_add_co_u32_e32 v20, vcc, 0x40000, v20
	s_nop 1
	v_addc_co_u32_e32 v21, vcc, 0, v21, vcc
	v_mul_f32_e32 v127, 0x3fb8aa3b, v127
	v_exp_f32_e32 v127, v127
	v_lshlrev_b32_e32 v24, 16, v94
	v_and_b32_e32 v25, 0xffff0000, v94
	v_lshlrev_b32_e32 v26, 16, v95
	v_and_b32_e32 v27, 0xffff0000, v95
	v_mov_b32_e32 v30, v127
	v_pk_fma_f32 v[10:11], v[10:11], v[30:31], v[24:25] op_sel_hi:[1,0,1]
	v_pk_fma_f32 v[12:13], v[12:13], v[30:31], v[26:27] op_sel_hi:[1,0,1]
	v_readlane_b32 s12, v253, 44
	s_nop 1
	v_add_u32_e32 v0, s12, v0
	s_mov_b32 s12, 0x1ffff
	v_cmp_lt_i32_e32 vcc, s12, v0
	v_readlane_b32 s12, v254, 27
	s_or_b64 s[10:11], vcc, s[10:11]
	s_nop 0
	v_add_u32_e32 v14, s12, v14
	s_andn2_b64 exec, exec, s[10:11]
	s_cbranch_execnz .LBB0_461
